# DSA select scan: ballots read the SGPR compare mask directly instead of re-deriving it through v_cndmask + v_cmp_ne (88 sites), on top of v048
# speedup vs baseline: 1.0103x; 1.0004x over previous
.LBB0_1108:
	s_or_b64 exec, exec, s[8:9]
	s_waitcnt lgkmcnt(0)
	v_add_u32_dpp v2, v0, v0 row_shr:1 row_mask:0xf bank_mask:0xf bound_ctrl:1
	v_add_u32_e32 v0, s33, v0
	s_mov_b32 s49, 0
	v_add_u32_dpp v2, v2, v2 row_shr:2 row_mask:0xf bank_mask:0xf bound_ctrl:1
	s_nop 1
	v_add_u32_dpp v2, v2, v2 row_shr:4 row_mask:0xf bank_mask:0xf bound_ctrl:1
	s_nop 1
	v_add_u32_dpp v2, v2, v2 row_shr:8 row_mask:0xf bank_mask:0xf bound_ctrl:1
	s_nop 1
	v_add_u32_dpp v2, v2, v2 row_bcast:15 row_mask:0xa bank_mask:0xf
	s_nop 1
	v_add_u32_dpp v2, v2, v2 row_bcast:31 row_mask:0xc bank_mask:0xf
	s_nop 0
	v_readlane_b32 s8, v2, 63
	v_add_u32_e32 v2, s44, v2
	v_sub_u32_e32 v0, v0, v2
	v_add_u32_e32 v0, s8, v0
	s_movk_i32 s8, 0xff
	v_cmp_lt_u32_e64 s[44:45], s8, v0
	s_and_b64 s[8:9], vcc, s[44:45]
	s_mov_b64 vcc, s[8:9]
	s_flbit_i32_b64 s8, vcc
	s_lshl_b32 s8, s8, 6
	s_xor_b32 s8, s8, 0xfc0
	s_cmp_lg_u64 vcc, 0
	s_cselect_b32 s93, s8, 0
	s_waitcnt vmcnt(16)
	v_mov_b32_e32 v14, v1
	v_mov_b32_e32 v15, v1
	v_readlane_b32 s8, v255, 28
	s_lshl_b32 s4, s4, 10
	v_mov_b32_e32 v0, v1
	v_mov_b32_e32 v2, v1
	v_mov_b32_e32 v3, v1
	v_mov_b32_e32 v4, v1
	v_mov_b32_e32 v5, v1
	v_mov_b32_e32 v6, v1
	v_mov_b32_e32 v7, v1
	v_mov_b32_e32 v8, v1
	v_mov_b32_e32 v9, v1
	v_mov_b32_e32 v10, v1
	v_mov_b32_e32 v11, v1
	v_mov_b32_e32 v12, v1
	v_mov_b32_e32 v13, v1
	v_readlane_b32 s9, v255, 29
	v_mov_b64_e32 v[50:51], v[14:15]
	s_add_i32 s93, s93, s4
	s_mov_b32 s33, 0
	v_lshlrev_b32_e32 v70, 1, v64
	v_lshl_add_u64 v[68:69], v[64:65], 2, s[8:9]
	v_mov_b64_e32 v[48:49], v[12:13]
	v_mov_b64_e32 v[46:47], v[10:11]
	v_mov_b64_e32 v[44:45], v[8:9]
	v_mov_b64_e32 v[42:43], v[6:7]
	v_mov_b64_e32 v[40:41], v[4:5]
	v_mov_b64_e32 v[38:39], v[2:3]
	v_mov_b64_e32 v[36:37], v[0:1]
	s_waitcnt vmcnt(15)
	s_waitcnt vmcnt(14)
	s_waitcnt vmcnt(0)

.LBB0_1127:
	v_and_b32_e32 v3, 0xffff, v60
	v_lshrrev_b32_e32 v5, 16, v60
	v_cmp_gt_u32_e64 s[44:45], s11, v2
	v_cmp_le_u32_e32 vcc, s93, v3
	v_cmp_le_u32_e64 s[46:47], s93, v5
	s_and_b64 s[18:19], s[44:45], vcc
	v_cndmask_b32_e64 v0, 0, 1, s[18:19]
	s_and_b64 s[8:9], s[44:45], s[46:47]
	s_mov_b64 vcc, s[18:19]
	s_mov_b64 s[44:45], s[8:9]
	v_mbcnt_lo_u32_b32 v4, vcc_lo, 0
	v_mbcnt_hi_u32_b32 v4, vcc_hi, v4
	v_mbcnt_lo_u32_b32 v4, s44, v4
	s_min_u32 s46, s49, 0x2c0
	v_mbcnt_hi_u32_b32 v4, s45, v4
	s_lshl_b32 s47, s46, 3
	s_sub_i32 s59, 0x2c0, s46
	s_add_i32 s58, s88, s47
	v_cmp_gt_u32_e64 s[46:47], s59, v4
	s_and_b64 s[18:19], s[18:19], s[46:47]
	s_and_saveexec_b64 s[46:47], s[18:19]
	v_lshl_add_u32 v6, v4, 3, s58
	ds_write_b64 v6, v[2:3]
	s_or_b64 exec, exec, s[46:47]
	v_add_u32_e32 v0, v4, v0
	v_cmp_gt_u32_e64 s[46:47], s59, v0
	s_and_b64 s[18:19], s[8:9], s[46:47]
	s_and_saveexec_b64 s[8:9], s[18:19]
	v_lshl_add_u32 v0, v0, 3, s58
	v_add_u32_e32 v4, 1, v2
	ds_write_b64 v0, v[4:5]
	s_or_b64 exec, exec, s[8:9]
	s_bcnt1_i32_b64 s8, vcc
	s_bcnt1_i32_b64 s9, s[44:45]
	s_add_i32 s8, s49, s8
	s_add_i32 s49, s8, s9
	s_add_i32 s8, s33, 0x80
	s_cmp_gt_i32 s8, s10
	s_cbranch_scc1 .LBB0_1113
.LBB0_1132:
	v_and_b32_e32 v7, 0xffff, v63
	v_add_u32_e32 v6, 0x80, v2
	v_lshrrev_b32_e32 v5, 16, v63
	v_cmp_gt_u32_e64 s[44:45], s11, v6
	v_cmp_le_u32_e32 vcc, s93, v7
	v_cmp_le_u32_e64 s[46:47], s93, v5
	s_and_b64 s[18:19], s[44:45], vcc
	v_cndmask_b32_e64 v0, 0, 1, s[18:19]
	s_and_b64 s[8:9], s[44:45], s[46:47]
	s_mov_b64 vcc, s[18:19]
	s_mov_b64 s[44:45], s[8:9]
	v_mbcnt_lo_u32_b32 v3, vcc_lo, 0
	v_mbcnt_hi_u32_b32 v3, vcc_hi, v3
	v_mbcnt_lo_u32_b32 v3, s44, v3
	s_min_u32 s46, s49, 0x2c0
	v_mbcnt_hi_u32_b32 v3, s45, v3
	s_lshl_b32 s47, s46, 3
	s_sub_i32 s59, 0x2c0, s46
	s_add_i32 s58, s88, s47
	v_cmp_gt_u32_e64 s[46:47], s59, v3
	s_and_b64 s[18:19], s[18:19], s[46:47]
	s_and_saveexec_b64 s[46:47], s[18:19]
	v_lshl_add_u32 v4, v3, 3, s58
	ds_write_b64 v4, v[6:7]
	s_or_b64 exec, exec, s[46:47]
	v_add_u32_e32 v0, v3, v0
	v_cmp_gt_u32_e64 s[46:47], s59, v0
	s_and_b64 s[18:19], s[8:9], s[46:47]
	s_and_saveexec_b64 s[8:9], s[18:19]
	v_lshl_add_u32 v0, v0, 3, s58
	v_add_u32_e32 v4, 0x81, v2
	ds_write_b64 v0, v[4:5]
	s_or_b64 exec, exec, s[8:9]
	s_bcnt1_i32_b64 s8, vcc
	s_bcnt1_i32_b64 s9, s[44:45]
	s_add_i32 s8, s49, s8
	s_add_i32 s49, s8, s9
	s_add_i32 s8, s33, 0x100
	s_cmp_gt_i32 s8, s10
	s_cbranch_scc1 .LBB0_1114
.LBB0_1137:
	v_and_b32_e32 v7, 0xffff, v62
	v_add_u32_e32 v6, 0x100, v2
	v_lshrrev_b32_e32 v5, 16, v62
	v_cmp_gt_u32_e64 s[44:45], s11, v6
	v_cmp_le_u32_e32 vcc, s93, v7
	v_cmp_le_u32_e64 s[46:47], s93, v5
	s_and_b64 s[18:19], s[44:45], vcc
	v_cndmask_b32_e64 v0, 0, 1, s[18:19]
	s_and_b64 s[8:9], s[44:45], s[46:47]
	s_mov_b64 vcc, s[18:19]
	s_mov_b64 s[44:45], s[8:9]
	v_mbcnt_lo_u32_b32 v3, vcc_lo, 0
	v_mbcnt_hi_u32_b32 v3, vcc_hi, v3
	v_mbcnt_lo_u32_b32 v3, s44, v3
	s_min_u32 s46, s49, 0x2c0
	v_mbcnt_hi_u32_b32 v3, s45, v3
	s_lshl_b32 s47, s46, 3
	s_sub_i32 s59, 0x2c0, s46
	s_add_i32 s58, s88, s47
	v_cmp_gt_u32_e64 s[46:47], s59, v3
	s_and_b64 s[18:19], s[18:19], s[46:47]
	s_and_saveexec_b64 s[46:47], s[18:19]
	v_lshl_add_u32 v4, v3, 3, s58
	ds_write_b64 v4, v[6:7]
	s_or_b64 exec, exec, s[46:47]
	v_add_u32_e32 v0, v3, v0
	v_cmp_gt_u32_e64 s[46:47], s59, v0
	s_and_b64 s[18:19], s[8:9], s[46:47]
	s_and_saveexec_b64 s[8:9], s[18:19]
	v_lshl_add_u32 v0, v0, 3, s58
	v_add_u32_e32 v4, 0x101, v2
	ds_write_b64 v0, v[4:5]
	s_or_b64 exec, exec, s[8:9]
	s_bcnt1_i32_b64 s8, vcc
	s_bcnt1_i32_b64 s9, s[44:45]
	s_add_i32 s8, s49, s8
	s_add_i32 s49, s8, s9
	s_add_i32 s8, s33, 0x180
	s_cmp_gt_i32 s8, s10
	s_cbranch_scc1 .LBB0_1115
.LBB0_1142:
	v_and_b32_e32 v7, 0xffff, v61
	v_add_u32_e32 v6, 0x180, v2
	v_lshrrev_b32_e32 v5, 16, v61
	v_cmp_gt_u32_e64 s[44:45], s11, v6
	v_cmp_le_u32_e32 vcc, s93, v7
	v_cmp_le_u32_e64 s[46:47], s93, v5
	s_and_b64 s[18:19], s[44:45], vcc
	v_cndmask_b32_e64 v0, 0, 1, s[18:19]
	s_and_b64 s[8:9], s[44:45], s[46:47]
	s_mov_b64 vcc, s[18:19]
	s_mov_b64 s[44:45], s[8:9]
	v_mbcnt_lo_u32_b32 v3, vcc_lo, 0
	v_mbcnt_hi_u32_b32 v3, vcc_hi, v3
	v_mbcnt_lo_u32_b32 v3, s44, v3
	s_min_u32 s46, s49, 0x2c0
	v_mbcnt_hi_u32_b32 v3, s45, v3
	s_lshl_b32 s47, s46, 3
	s_sub_i32 s59, 0x2c0, s46
	s_add_i32 s58, s88, s47
	v_cmp_gt_u32_e64 s[46:47], s59, v3
	s_and_b64 s[18:19], s[18:19], s[46:47]
	s_and_saveexec_b64 s[46:47], s[18:19]
	v_lshl_add_u32 v4, v3, 3, s58
	ds_write_b64 v4, v[6:7]
	s_or_b64 exec, exec, s[46:47]
	v_add_u32_e32 v0, v3, v0
	v_cmp_gt_u32_e64 s[46:47], s59, v0
	s_and_b64 s[18:19], s[8:9], s[46:47]
	s_and_saveexec_b64 s[8:9], s[18:19]
	v_lshl_add_u32 v0, v0, 3, s58
	v_add_u32_e32 v4, 0x181, v2
	ds_write_b64 v0, v[4:5]
	s_or_b64 exec, exec, s[8:9]
	s_bcnt1_i32_b64 s8, vcc
	s_bcnt1_i32_b64 s9, s[44:45]
	s_add_i32 s8, s49, s8
	s_add_i32 s49, s8, s9
	s_add_i32 s8, s33, 0x200
	s_cmp_gt_i32 s8, s10
	s_cbranch_scc1 .LBB0_1116
.LBB0_1147:
	v_and_b32_e32 v7, 0xffff, v58
	v_add_u32_e32 v6, 0x200, v2
	v_lshrrev_b32_e32 v5, 16, v58
	v_cmp_gt_u32_e64 s[44:45], s11, v6
	v_cmp_le_u32_e32 vcc, s93, v7
	v_cmp_le_u32_e64 s[46:47], s93, v5
	s_and_b64 s[18:19], s[44:45], vcc
	v_cndmask_b32_e64 v0, 0, 1, s[18:19]
	s_and_b64 s[8:9], s[44:45], s[46:47]
	s_mov_b64 vcc, s[18:19]
	s_mov_b64 s[44:45], s[8:9]
	v_mbcnt_lo_u32_b32 v3, vcc_lo, 0
	v_mbcnt_hi_u32_b32 v3, vcc_hi, v3
	v_mbcnt_lo_u32_b32 v3, s44, v3
	s_min_u32 s46, s49, 0x2c0
	v_mbcnt_hi_u32_b32 v3, s45, v3
	s_lshl_b32 s47, s46, 3
	s_sub_i32 s59, 0x2c0, s46
	s_add_i32 s58, s88, s47
	v_cmp_gt_u32_e64 s[46:47], s59, v3
	s_and_b64 s[18:19], s[18:19], s[46:47]
	s_and_saveexec_b64 s[46:47], s[18:19]
	v_lshl_add_u32 v4, v3, 3, s58
	ds_write_b64 v4, v[6:7]
	s_or_b64 exec, exec, s[46:47]
	v_add_u32_e32 v0, v3, v0
	v_cmp_gt_u32_e64 s[46:47], s59, v0
	s_and_b64 s[18:19], s[8:9], s[46:47]
	s_and_saveexec_b64 s[8:9], s[18:19]
	v_lshl_add_u32 v0, v0, 3, s58
	v_add_u32_e32 v4, 0x201, v2
	ds_write_b64 v0, v[4:5]
	s_or_b64 exec, exec, s[8:9]
	s_bcnt1_i32_b64 s8, vcc
	s_bcnt1_i32_b64 s9, s[44:45]
	s_add_i32 s8, s49, s8
	s_add_i32 s49, s8, s9
	s_add_i32 s8, s33, 0x280
	s_cmp_gt_i32 s8, s10
	s_cbranch_scc1 .LBB0_1117
.LBB0_1152:
	v_and_b32_e32 v7, 0xffff, v59
	v_add_u32_e32 v6, 0x280, v2
	v_lshrrev_b32_e32 v5, 16, v59
	v_cmp_gt_u32_e64 s[44:45], s11, v6
	v_cmp_le_u32_e32 vcc, s93, v7
	v_cmp_le_u32_e64 s[46:47], s93, v5
	s_and_b64 s[18:19], s[44:45], vcc
	v_cndmask_b32_e64 v0, 0, 1, s[18:19]
	s_and_b64 s[8:9], s[44:45], s[46:47]
	s_mov_b64 vcc, s[18:19]
	s_mov_b64 s[44:45], s[8:9]
	v_mbcnt_lo_u32_b32 v3, vcc_lo, 0
	v_mbcnt_hi_u32_b32 v3, vcc_hi, v3
	v_mbcnt_lo_u32_b32 v3, s44, v3
	s_min_u32 s46, s49, 0x2c0
	v_mbcnt_hi_u32_b32 v3, s45, v3
	s_lshl_b32 s47, s46, 3
	s_sub_i32 s59, 0x2c0, s46
	s_add_i32 s58, s88, s47
	v_cmp_gt_u32_e64 s[46:47], s59, v3
	s_and_b64 s[18:19], s[18:19], s[46:47]
	s_and_saveexec_b64 s[46:47], s[18:19]
	v_lshl_add_u32 v4, v3, 3, s58
	ds_write_b64 v4, v[6:7]
	s_or_b64 exec, exec, s[46:47]
	v_add_u32_e32 v0, v3, v0
	v_cmp_gt_u32_e64 s[46:47], s59, v0
	s_and_b64 s[18:19], s[8:9], s[46:47]
	s_and_saveexec_b64 s[8:9], s[18:19]
	v_lshl_add_u32 v0, v0, 3, s58
	v_add_u32_e32 v4, 0x281, v2
	ds_write_b64 v0, v[4:5]
	s_or_b64 exec, exec, s[8:9]
	s_bcnt1_i32_b64 s8, vcc
	s_bcnt1_i32_b64 s9, s[44:45]
	s_add_i32 s8, s49, s8
	s_add_i32 s49, s8, s9
	s_add_i32 s8, s33, 0x300
	s_cmp_gt_i32 s8, s10
	s_cbranch_scc1 .LBB0_1118
.LBB0_1157:
	v_and_b32_e32 v7, 0xffff, v56
	v_add_u32_e32 v6, 0x300, v2
	v_lshrrev_b32_e32 v5, 16, v56
	v_cmp_gt_u32_e64 s[44:45], s11, v6
	v_cmp_le_u32_e32 vcc, s93, v7
	v_cmp_le_u32_e64 s[46:47], s93, v5
	s_and_b64 s[18:19], s[44:45], vcc
	v_cndmask_b32_e64 v0, 0, 1, s[18:19]
	s_and_b64 s[8:9], s[44:45], s[46:47]
	s_mov_b64 vcc, s[18:19]
	s_mov_b64 s[44:45], s[8:9]
	v_mbcnt_lo_u32_b32 v3, vcc_lo, 0
	v_mbcnt_hi_u32_b32 v3, vcc_hi, v3
	v_mbcnt_lo_u32_b32 v3, s44, v3
	s_min_u32 s46, s49, 0x2c0
	v_mbcnt_hi_u32_b32 v3, s45, v3
	s_lshl_b32 s47, s46, 3
	s_sub_i32 s59, 0x2c0, s46
	s_add_i32 s58, s88, s47
	v_cmp_gt_u32_e64 s[46:47], s59, v3
	s_and_b64 s[18:19], s[18:19], s[46:47]
	s_and_saveexec_b64 s[46:47], s[18:19]
	v_lshl_add_u32 v4, v3, 3, s58
	ds_write_b64 v4, v[6:7]
	s_or_b64 exec, exec, s[46:47]
	v_add_u32_e32 v0, v3, v0
	v_cmp_gt_u32_e64 s[46:47], s59, v0
	s_and_b64 s[18:19], s[8:9], s[46:47]
	s_and_saveexec_b64 s[8:9], s[18:19]
	v_lshl_add_u32 v0, v0, 3, s58
	v_add_u32_e32 v4, 0x301, v2
	ds_write_b64 v0, v[4:5]
	s_or_b64 exec, exec, s[8:9]
	s_bcnt1_i32_b64 s8, vcc
	s_bcnt1_i32_b64 s9, s[44:45]
	s_add_i32 s8, s49, s8
	s_add_i32 s49, s8, s9
	s_add_i32 s8, s33, 0x380
	s_cmp_gt_i32 s8, s10
	s_cbranch_scc1 .LBB0_1119
.LBB0_1162:
	v_and_b32_e32 v7, 0xffff, v57
	v_add_u32_e32 v6, 0x380, v2
	v_lshrrev_b32_e32 v5, 16, v57
	v_cmp_gt_u32_e64 s[44:45], s11, v6
	v_cmp_le_u32_e32 vcc, s93, v7
	v_cmp_le_u32_e64 s[46:47], s93, v5
	s_and_b64 s[18:19], s[44:45], vcc
	v_cndmask_b32_e64 v0, 0, 1, s[18:19]
	s_and_b64 s[8:9], s[44:45], s[46:47]
	s_mov_b64 vcc, s[18:19]
	s_mov_b64 s[44:45], s[8:9]
	v_mbcnt_lo_u32_b32 v3, vcc_lo, 0
	v_mbcnt_hi_u32_b32 v3, vcc_hi, v3
	v_mbcnt_lo_u32_b32 v3, s44, v3
	s_min_u32 s46, s49, 0x2c0
	v_mbcnt_hi_u32_b32 v3, s45, v3
	s_lshl_b32 s47, s46, 3
	s_sub_i32 s59, 0x2c0, s46
	s_add_i32 s58, s88, s47
	v_cmp_gt_u32_e64 s[46:47], s59, v3
	s_and_b64 s[18:19], s[18:19], s[46:47]
	s_and_saveexec_b64 s[46:47], s[18:19]
	v_lshl_add_u32 v4, v3, 3, s58
	ds_write_b64 v4, v[6:7]
	s_or_b64 exec, exec, s[46:47]
	v_add_u32_e32 v0, v3, v0
	v_cmp_gt_u32_e64 s[46:47], s59, v0
	s_and_b64 s[18:19], s[8:9], s[46:47]
	s_and_saveexec_b64 s[8:9], s[18:19]
	v_lshl_add_u32 v0, v0, 3, s58
	v_add_u32_e32 v4, 0x381, v2
	ds_write_b64 v0, v[4:5]
	s_or_b64 exec, exec, s[8:9]
	s_bcnt1_i32_b64 s8, vcc
	s_bcnt1_i32_b64 s9, s[44:45]
	s_add_i32 s8, s49, s8
	s_add_i32 s49, s8, s9
	s_add_i32 s8, s33, 0x400
	s_cmp_gt_i32 s8, s10
	s_cbranch_scc1 .LBB0_1120
.LBB0_1167:
	v_and_b32_e32 v7, 0xffff, v54
	v_add_u32_e32 v6, 0x400, v2
	v_lshrrev_b32_e32 v5, 16, v54
	v_cmp_gt_u32_e64 s[44:45], s11, v6
	v_cmp_le_u32_e32 vcc, s93, v7
	v_cmp_le_u32_e64 s[46:47], s93, v5
	s_and_b64 s[18:19], s[44:45], vcc
	v_cndmask_b32_e64 v0, 0, 1, s[18:19]
	s_and_b64 s[8:9], s[44:45], s[46:47]
	s_mov_b64 vcc, s[18:19]
	s_mov_b64 s[44:45], s[8:9]
	v_mbcnt_lo_u32_b32 v3, vcc_lo, 0
	v_mbcnt_hi_u32_b32 v3, vcc_hi, v3
	v_mbcnt_lo_u32_b32 v3, s44, v3
	s_min_u32 s46, s49, 0x2c0
	v_mbcnt_hi_u32_b32 v3, s45, v3
	s_lshl_b32 s47, s46, 3
	s_sub_i32 s59, 0x2c0, s46
	s_add_i32 s58, s88, s47
	v_cmp_gt_u32_e64 s[46:47], s59, v3
	s_and_b64 s[18:19], s[18:19], s[46:47]
	s_and_saveexec_b64 s[46:47], s[18:19]
	v_lshl_add_u32 v4, v3, 3, s58
	ds_write_b64 v4, v[6:7]
	s_or_b64 exec, exec, s[46:47]
	v_add_u32_e32 v0, v3, v0
	v_cmp_gt_u32_e64 s[46:47], s59, v0
	s_and_b64 s[18:19], s[8:9], s[46:47]
	s_and_saveexec_b64 s[8:9], s[18:19]
	v_lshl_add_u32 v0, v0, 3, s58
	v_add_u32_e32 v4, 0x401, v2
	ds_write_b64 v0, v[4:5]
	s_or_b64 exec, exec, s[8:9]
	s_bcnt1_i32_b64 s8, vcc
	s_bcnt1_i32_b64 s9, s[44:45]
	s_add_i32 s8, s49, s8
	s_add_i32 s49, s8, s9
	s_add_i32 s8, s33, 0x480
	s_cmp_gt_i32 s8, s10
	s_cbranch_scc1 .LBB0_1121
.LBB0_1172:
	v_and_b32_e32 v7, 0xffff, v55
	v_add_u32_e32 v6, 0x480, v2
	v_lshrrev_b32_e32 v5, 16, v55
	v_cmp_gt_u32_e64 s[44:45], s11, v6
	v_cmp_le_u32_e32 vcc, s93, v7
	v_cmp_le_u32_e64 s[46:47], s93, v5
	s_and_b64 s[18:19], s[44:45], vcc
	v_cndmask_b32_e64 v0, 0, 1, s[18:19]
	s_and_b64 s[8:9], s[44:45], s[46:47]
	s_mov_b64 vcc, s[18:19]
	s_mov_b64 s[44:45], s[8:9]
	v_mbcnt_lo_u32_b32 v3, vcc_lo, 0
	v_mbcnt_hi_u32_b32 v3, vcc_hi, v3
	v_mbcnt_lo_u32_b32 v3, s44, v3
	s_min_u32 s46, s49, 0x2c0
	v_mbcnt_hi_u32_b32 v3, s45, v3
	s_lshl_b32 s47, s46, 3
	s_sub_i32 s59, 0x2c0, s46
	s_add_i32 s58, s88, s47
	v_cmp_gt_u32_e64 s[46:47], s59, v3
	s_and_b64 s[18:19], s[18:19], s[46:47]
	s_and_saveexec_b64 s[46:47], s[18:19]
	v_lshl_add_u32 v4, v3, 3, s58
	ds_write_b64 v4, v[6:7]
	s_or_b64 exec, exec, s[46:47]
	v_add_u32_e32 v0, v3, v0
	v_cmp_gt_u32_e64 s[46:47], s59, v0
	s_and_b64 s[18:19], s[8:9], s[46:47]
	s_and_saveexec_b64 s[8:9], s[18:19]
	v_lshl_add_u32 v0, v0, 3, s58
	v_add_u32_e32 v4, 0x481, v2
	ds_write_b64 v0, v[4:5]
	s_or_b64 exec, exec, s[8:9]
	s_bcnt1_i32_b64 s8, vcc
	s_bcnt1_i32_b64 s9, s[44:45]
	s_add_i32 s8, s49, s8
	s_add_i32 s49, s8, s9
	s_add_i32 s8, s33, 0x500
	s_cmp_gt_i32 s8, s10
	s_cbranch_scc1 .LBB0_1122
.LBB0_1177:
	v_and_b32_e32 v7, 0xffff, v52
	v_add_u32_e32 v6, 0x500, v2
	v_lshrrev_b32_e32 v5, 16, v52
	v_cmp_gt_u32_e64 s[44:45], s11, v6
	v_cmp_le_u32_e32 vcc, s93, v7
	v_cmp_le_u32_e64 s[46:47], s93, v5
	s_and_b64 s[18:19], s[44:45], vcc
	v_cndmask_b32_e64 v0, 0, 1, s[18:19]
	s_and_b64 s[8:9], s[44:45], s[46:47]
	s_mov_b64 vcc, s[18:19]
	s_mov_b64 s[44:45], s[8:9]
	v_mbcnt_lo_u32_b32 v3, vcc_lo, 0
	v_mbcnt_hi_u32_b32 v3, vcc_hi, v3
	v_mbcnt_lo_u32_b32 v3, s44, v3
	s_min_u32 s46, s49, 0x2c0
	v_mbcnt_hi_u32_b32 v3, s45, v3
	s_lshl_b32 s47, s46, 3
	s_sub_i32 s59, 0x2c0, s46
	s_add_i32 s58, s88, s47
	v_cmp_gt_u32_e64 s[46:47], s59, v3
	s_and_b64 s[18:19], s[18:19], s[46:47]
	s_and_saveexec_b64 s[46:47], s[18:19]
	v_lshl_add_u32 v4, v3, 3, s58
	ds_write_b64 v4, v[6:7]
	s_or_b64 exec, exec, s[46:47]
	v_add_u32_e32 v0, v3, v0
	v_cmp_gt_u32_e64 s[46:47], s59, v0
	s_and_b64 s[18:19], s[8:9], s[46:47]
	s_and_saveexec_b64 s[8:9], s[18:19]
	v_lshl_add_u32 v0, v0, 3, s58
	v_add_u32_e32 v4, 0x501, v2
	ds_write_b64 v0, v[4:5]
	s_or_b64 exec, exec, s[8:9]
	s_bcnt1_i32_b64 s8, vcc
	s_bcnt1_i32_b64 s9, s[44:45]
	s_add_i32 s8, s49, s8
	s_add_i32 s49, s8, s9
	s_add_i32 s8, s33, 0x580
	s_cmp_gt_i32 s8, s10
	s_cbranch_scc1 .LBB0_1123
.LBB0_1182:
	v_and_b32_e32 v7, 0xffff, v53
	v_add_u32_e32 v6, 0x580, v2
	v_lshrrev_b32_e32 v5, 16, v53
	v_cmp_gt_u32_e64 s[44:45], s11, v6
	v_cmp_le_u32_e32 vcc, s93, v7
	v_cmp_le_u32_e64 s[46:47], s93, v5
	s_and_b64 s[18:19], s[44:45], vcc
	v_cndmask_b32_e64 v0, 0, 1, s[18:19]
	s_and_b64 s[8:9], s[44:45], s[46:47]
	s_mov_b64 vcc, s[18:19]
	s_mov_b64 s[44:45], s[8:9]
	v_mbcnt_lo_u32_b32 v3, vcc_lo, 0
	v_mbcnt_hi_u32_b32 v3, vcc_hi, v3
	v_mbcnt_lo_u32_b32 v3, s44, v3
	s_min_u32 s46, s49, 0x2c0
	v_mbcnt_hi_u32_b32 v3, s45, v3
	s_lshl_b32 s47, s46, 3
	s_sub_i32 s59, 0x2c0, s46
	s_add_i32 s58, s88, s47
	v_cmp_gt_u32_e64 s[46:47], s59, v3
	s_and_b64 s[18:19], s[18:19], s[46:47]
	s_and_saveexec_b64 s[46:47], s[18:19]
	v_lshl_add_u32 v4, v3, 3, s58
	ds_write_b64 v4, v[6:7]
	s_or_b64 exec, exec, s[46:47]
	v_add_u32_e32 v0, v3, v0
	v_cmp_gt_u32_e64 s[46:47], s59, v0
	s_and_b64 s[18:19], s[8:9], s[46:47]
	s_and_saveexec_b64 s[8:9], s[18:19]
	v_lshl_add_u32 v0, v0, 3, s58
	v_add_u32_e32 v4, 0x581, v2
	ds_write_b64 v0, v[4:5]
	s_or_b64 exec, exec, s[8:9]
	s_bcnt1_i32_b64 s8, vcc
	s_bcnt1_i32_b64 s9, s[44:45]
	s_add_i32 s8, s49, s8
	s_add_i32 s49, s8, s9
	s_add_i32 s8, s33, 0x600
	s_cmp_gt_i32 s8, s10
	s_cbranch_scc1 .LBB0_1124
.LBB0_1187:
	v_and_b32_e32 v7, 0xffff, v34
	v_add_u32_e32 v6, 0x600, v2
	v_lshrrev_b32_e32 v5, 16, v34
	v_cmp_gt_u32_e64 s[44:45], s11, v6
	v_cmp_le_u32_e32 vcc, s93, v7
	v_cmp_le_u32_e64 s[46:47], s93, v5
	s_and_b64 s[18:19], s[44:45], vcc
	v_cndmask_b32_e64 v0, 0, 1, s[18:19]
	s_and_b64 s[8:9], s[44:45], s[46:47]
	s_mov_b64 vcc, s[18:19]
	s_mov_b64 s[44:45], s[8:9]
	v_mbcnt_lo_u32_b32 v3, vcc_lo, 0
	v_mbcnt_hi_u32_b32 v3, vcc_hi, v3
	v_mbcnt_lo_u32_b32 v3, s44, v3
	s_min_u32 s46, s49, 0x2c0
	v_mbcnt_hi_u32_b32 v3, s45, v3
	s_lshl_b32 s47, s46, 3
	s_sub_i32 s59, 0x2c0, s46
	s_add_i32 s58, s88, s47
	v_cmp_gt_u32_e64 s[46:47], s59, v3
	s_and_b64 s[18:19], s[18:19], s[46:47]
	s_and_saveexec_b64 s[46:47], s[18:19]
	v_lshl_add_u32 v4, v3, 3, s58
	ds_write_b64 v4, v[6:7]
	s_or_b64 exec, exec, s[46:47]
	v_add_u32_e32 v0, v3, v0
	v_cmp_gt_u32_e64 s[46:47], s59, v0
	s_and_b64 s[18:19], s[8:9], s[46:47]
	s_and_saveexec_b64 s[8:9], s[18:19]
	v_lshl_add_u32 v0, v0, 3, s58
	v_add_u32_e32 v4, 0x601, v2
	ds_write_b64 v0, v[4:5]
	s_or_b64 exec, exec, s[8:9]
	s_bcnt1_i32_b64 s8, vcc
	s_bcnt1_i32_b64 s9, s[44:45]
	s_add_i32 s8, s49, s8
	s_add_i32 s49, s8, s9
	s_add_i32 s8, s33, 0x680
	s_cmp_gt_i32 s8, s10
	s_cbranch_scc1 .LBB0_1125
.LBB0_1192:
	v_and_b32_e32 v7, 0xffff, v35
	v_add_u32_e32 v6, 0x680, v2
	v_lshrrev_b32_e32 v5, 16, v35
	v_cmp_gt_u32_e64 s[44:45], s11, v6
	v_cmp_le_u32_e32 vcc, s93, v7
	v_cmp_le_u32_e64 s[46:47], s93, v5
	s_and_b64 s[18:19], s[44:45], vcc
	v_cndmask_b32_e64 v0, 0, 1, s[18:19]
	s_and_b64 s[8:9], s[44:45], s[46:47]
	s_mov_b64 vcc, s[18:19]
	s_mov_b64 s[44:45], s[8:9]
	v_mbcnt_lo_u32_b32 v3, vcc_lo, 0
	v_mbcnt_hi_u32_b32 v3, vcc_hi, v3
	v_mbcnt_lo_u32_b32 v3, s44, v3
	s_min_u32 s46, s49, 0x2c0
	v_mbcnt_hi_u32_b32 v3, s45, v3
	s_lshl_b32 s47, s46, 3
	s_sub_i32 s59, 0x2c0, s46
	s_add_i32 s58, s88, s47
	v_cmp_gt_u32_e64 s[46:47], s59, v3
	s_and_b64 s[18:19], s[18:19], s[46:47]
	s_and_saveexec_b64 s[46:47], s[18:19]
	v_lshl_add_u32 v4, v3, 3, s58
	ds_write_b64 v4, v[6:7]
	s_or_b64 exec, exec, s[46:47]
	v_add_u32_e32 v0, v3, v0
	v_cmp_gt_u32_e64 s[46:47], s59, v0
	s_and_b64 s[18:19], s[8:9], s[46:47]
	s_and_saveexec_b64 s[8:9], s[18:19]
	v_lshl_add_u32 v0, v0, 3, s58
	v_add_u32_e32 v4, 0x681, v2
	ds_write_b64 v0, v[4:5]
	s_or_b64 exec, exec, s[8:9]
	s_bcnt1_i32_b64 s8, vcc
	s_bcnt1_i32_b64 s9, s[44:45]
	s_add_i32 s8, s49, s8
	s_add_i32 s49, s8, s9
	s_add_i32 s8, s33, 0x700
	s_cmp_gt_i32 s8, s10
	s_cbranch_scc1 .LBB0_1126
.LBB0_1197:
	v_and_b32_e32 v7, 0xffff, v32
	v_add_u32_e32 v6, 0x700, v2
	v_lshrrev_b32_e32 v5, 16, v32
	v_cmp_gt_u32_e64 s[44:45], s11, v6
	v_cmp_le_u32_e32 vcc, s93, v7
	v_cmp_le_u32_e64 s[46:47], s93, v5
	s_and_b64 s[18:19], s[44:45], vcc
	v_cndmask_b32_e64 v0, 0, 1, s[18:19]
	s_and_b64 s[8:9], s[44:45], s[46:47]
	s_mov_b64 vcc, s[18:19]
	s_mov_b64 s[44:45], s[8:9]
	v_mbcnt_lo_u32_b32 v3, vcc_lo, 0
	v_mbcnt_hi_u32_b32 v3, vcc_hi, v3
	v_mbcnt_lo_u32_b32 v3, s44, v3
	s_min_u32 s46, s49, 0x2c0
	v_mbcnt_hi_u32_b32 v3, s45, v3
	s_lshl_b32 s47, s46, 3
	s_sub_i32 s59, 0x2c0, s46
	s_add_i32 s58, s88, s47
	v_cmp_gt_u32_e64 s[46:47], s59, v3
	s_and_b64 s[18:19], s[18:19], s[46:47]
	s_and_saveexec_b64 s[46:47], s[18:19]
	v_lshl_add_u32 v4, v3, 3, s58
	ds_write_b64 v4, v[6:7]
	s_or_b64 exec, exec, s[46:47]
	v_add_u32_e32 v0, v3, v0
	v_cmp_gt_u32_e64 s[46:47], s59, v0
	s_and_b64 s[18:19], s[8:9], s[46:47]
	s_and_saveexec_b64 s[8:9], s[18:19]
	v_lshl_add_u32 v0, v0, 3, s58
	v_add_u32_e32 v4, 0x701, v2
	ds_write_b64 v0, v[4:5]
	s_or_b64 exec, exec, s[8:9]
	s_bcnt1_i32_b64 s8, vcc
	s_bcnt1_i32_b64 s9, s[44:45]
	s_add_i32 s8, s49, s8
	s_add_i32 s49, s8, s9
	s_add_i32 s8, s33, 0x780
	s_cmp_gt_i32 s8, s10
	s_cbranch_scc1 .LBB0_1207
.LBB0_1202:
	v_and_b32_e32 v5, 0xffff, v33
	v_add_u32_e32 v4, 0x780, v2
	v_lshrrev_b32_e32 v3, 16, v33
	v_cmp_gt_u32_e64 s[44:45], s11, v4
	v_cmp_le_u32_e32 vcc, s93, v5
	v_cmp_le_u32_e64 s[46:47], s93, v3
	s_and_b64 s[18:19], s[44:45], vcc
	v_cndmask_b32_e64 v0, 0, 1, s[18:19]
	s_and_b64 s[8:9], s[44:45], s[46:47]
	s_mov_b64 vcc, s[18:19]
	s_mov_b64 s[44:45], s[8:9]
	v_mbcnt_lo_u32_b32 v6, vcc_lo, 0
	v_mbcnt_hi_u32_b32 v6, vcc_hi, v6
	v_mbcnt_lo_u32_b32 v6, s44, v6
	s_min_u32 s46, s49, 0x2c0
	v_mbcnt_hi_u32_b32 v6, s45, v6
	s_sub_i32 s58, 0x2c0, s46
	s_lshl_b32 s33, s46, 3
	v_cmp_gt_u32_e64 s[46:47], s58, v6
	s_add_i32 s33, s88, s33
	s_and_b64 s[18:19], s[18:19], s[46:47]
	s_and_saveexec_b64 s[46:47], s[18:19]
	v_lshl_add_u32 v7, v6, 3, s33
	ds_write_b64 v7, v[4:5]
	s_or_b64 exec, exec, s[46:47]
	v_add_u32_e32 v0, v6, v0
	v_cmp_gt_u32_e64 s[46:47], s58, v0
	s_and_b64 s[18:19], s[8:9], s[46:47]
	s_and_saveexec_b64 s[8:9], s[18:19]
	v_lshl_add_u32 v0, v0, 3, s33
	v_add_u32_e32 v2, 0x781, v2
	ds_write_b64 v0, v[2:3]
	s_or_b64 exec, exec, s[8:9]
	s_bcnt1_i32_b64 s8, vcc
	s_bcnt1_i32_b64 s9, s[44:45]
	s_add_i32 s8, s49, s8
	s_add_i32 s49, s8, s9

.LBB0_1211:
	s_or_b64 exec, exec, s[6:7]
	s_waitcnt lgkmcnt(0)
	v_add_u32_dpp v2, v0, v0 row_shr:1 row_mask:0xf bank_mask:0xf bound_ctrl:1
	v_add_u32_e32 v0, s8, v0
	s_mov_b32 s28, 0
	v_add_u32_dpp v2, v2, v2 row_shr:2 row_mask:0xf bank_mask:0xf bound_ctrl:1
	s_nop 1
	v_add_u32_dpp v2, v2, v2 row_shr:4 row_mask:0xf bank_mask:0xf bound_ctrl:1
	s_nop 1
	v_add_u32_dpp v2, v2, v2 row_shr:8 row_mask:0xf bank_mask:0xf bound_ctrl:1
	s_nop 1
	v_add_u32_dpp v2, v2, v2 row_bcast:15 row_mask:0xa bank_mask:0xf
	s_nop 1
	v_add_u32_dpp v2, v2, v2 row_bcast:31 row_mask:0xc bank_mask:0xf
	s_nop 0
	v_readlane_b32 s6, v2, 63
	v_add_u32_e32 v2, s9, v2
	v_sub_u32_e32 v0, v0, v2
	v_add_u32_e32 v0, s6, v0
	s_movk_i32 s6, 0xff
	v_cmp_lt_u32_e64 s[44:45], s6, v0
	s_and_b64 s[6:7], vcc, s[44:45]
	s_mov_b64 vcc, s[6:7]
	s_flbit_i32_b64 s6, vcc
	s_lshl_b32 s6, s6, 6
	s_xor_b32 s6, s6, 0xfc0
	s_cmp_lg_u64 vcc, 0
	s_cselect_b32 s29, s6, 0
	v_ashrrev_i32_e32 v65, 31, v64
	v_lshlrev_b64 v[2:3], 2, v[64:65]
	v_mov_b32_e32 v14, v1
	v_mov_b32_e32 v15, v1
	s_lshl_b32 s4, s4, 10
	v_lshl_add_u64 v[66:67], s[14:15], 0, v[2:3]
	v_lshl_add_u64 v[68:69], s[20:21], 0, v[2:3]
	v_mov_b32_e32 v0, v1
	v_mov_b32_e32 v2, v1
	v_mov_b32_e32 v3, v1
	v_mov_b32_e32 v4, v1
	v_mov_b32_e32 v5, v1
	v_mov_b32_e32 v6, v1
	v_mov_b32_e32 v7, v1
	v_mov_b32_e32 v8, v1
	v_mov_b32_e32 v9, v1
	v_mov_b32_e32 v10, v1
	v_mov_b32_e32 v11, v1
	v_mov_b32_e32 v12, v1
	v_mov_b32_e32 v13, v1
	v_mov_b64_e32 v[62:63], v[14:15]
	v_mov_b32_e32 v16, v32
	v_mov_b32_e32 v17, v33
	v_mov_b32_e32 v18, v34
	v_mov_b32_e32 v19, v35
	v_mov_b32_e32 v20, v36
	v_mov_b32_e32 v21, v37
	v_mov_b32_e32 v22, v38
	v_mov_b32_e32 v23, v39
	v_mov_b32_e32 v24, v40
	v_mov_b32_e32 v25, v41
	v_mov_b32_e32 v26, v42
	v_mov_b32_e32 v27, v43
	v_mov_b32_e32 v28, v44
	v_mov_b32_e32 v29, v45
	v_mov_b32_e32 v30, v46
	v_mov_b32_e32 v31, v47
	s_add_i32 s29, s29, s4
	v_lshlrev_b32_e32 v70, 1, v64
	s_mov_b32 s30, 0
	v_mov_b64_e32 v[60:61], v[12:13]
	v_mov_b64_e32 v[58:59], v[10:11]
	v_mov_b64_e32 v[56:57], v[8:9]
	v_mov_b64_e32 v[54:55], v[6:7]
	v_mov_b64_e32 v[52:53], v[4:5]
	v_mov_b64_e32 v[50:51], v[2:3]
	v_mov_b64_e32 v[48:49], v[0:1]

.LBB0_1230:
	v_and_b32_e32 v3, 0xffff, v16
	v_lshrrev_b32_e32 v5, 16, v16
	v_cmp_gt_u32_e64 s[44:45], s11, v2
	v_cmp_le_u32_e32 vcc, s29, v3
	v_cmp_le_u32_e64 s[46:47], s29, v5
	s_and_b64 s[18:19], s[44:45], vcc
	v_cndmask_b32_e64 v0, 0, 1, s[18:19]
	s_and_b64 s[8:9], s[44:45], s[46:47]
	s_mov_b64 vcc, s[18:19]
	s_mov_b64 s[44:45], s[8:9]
	v_mbcnt_lo_u32_b32 v4, vcc_lo, 0
	v_mbcnt_hi_u32_b32 v4, vcc_hi, v4
	v_mbcnt_lo_u32_b32 v4, s44, v4
	s_min_u32 s26, s28, 0x2c0
	v_mbcnt_hi_u32_b32 v4, s45, v4
	s_sub_i32 s33, 0x2c0, s26
	s_lshl_b32 s27, s26, 3
	v_cmp_gt_u32_e64 s[46:47], s33, v4
	s_add_i32 s31, s88, s27
	s_and_b64 s[18:19], s[18:19], s[46:47]
	s_and_saveexec_b64 s[26:27], s[18:19]
	v_lshl_add_u32 v6, v4, 3, s31
	ds_write_b64 v6, v[2:3]
	s_or_b64 exec, exec, s[26:27]
	v_add_u32_e32 v0, v4, v0
	v_cmp_gt_u32_e64 s[46:47], s33, v0
	s_and_b64 s[18:19], s[8:9], s[46:47]
	s_and_saveexec_b64 s[8:9], s[18:19]
	v_lshl_add_u32 v0, v0, 3, s31
	v_add_u32_e32 v4, 1, v2
	ds_write_b64 v0, v[4:5]
	s_or_b64 exec, exec, s[8:9]
	s_bcnt1_i32_b64 s8, vcc
	s_bcnt1_i32_b64 s9, s[44:45]
	s_add_i32 s8, s28, s8
	s_add_i32 s28, s8, s9
	s_add_i32 s8, s30, 0x80
	s_cmp_gt_i32 s8, s10
	s_cbranch_scc1 .LBB0_1216
.LBB0_1235:
	v_and_b32_e32 v7, 0xffff, v17
	v_add_u32_e32 v6, 0x80, v2
	v_lshrrev_b32_e32 v5, 16, v17
	v_cmp_gt_u32_e64 s[44:45], s11, v6
	v_cmp_le_u32_e32 vcc, s29, v7
	v_cmp_le_u32_e64 s[46:47], s29, v5
	s_and_b64 s[18:19], s[44:45], vcc
	v_cndmask_b32_e64 v0, 0, 1, s[18:19]
	s_and_b64 s[8:9], s[44:45], s[46:47]
	s_mov_b64 vcc, s[18:19]
	s_mov_b64 s[44:45], s[8:9]
	v_mbcnt_lo_u32_b32 v3, vcc_lo, 0
	v_mbcnt_hi_u32_b32 v3, vcc_hi, v3
	v_mbcnt_lo_u32_b32 v3, s44, v3
	s_min_u32 s26, s28, 0x2c0
	v_mbcnt_hi_u32_b32 v3, s45, v3
	s_sub_i32 s33, 0x2c0, s26
	s_lshl_b32 s27, s26, 3
	v_cmp_gt_u32_e64 s[46:47], s33, v3
	s_add_i32 s31, s88, s27
	s_and_b64 s[18:19], s[18:19], s[46:47]
	s_and_saveexec_b64 s[26:27], s[18:19]
	v_lshl_add_u32 v4, v3, 3, s31
	ds_write_b64 v4, v[6:7]
	s_or_b64 exec, exec, s[26:27]
	v_add_u32_e32 v0, v3, v0
	v_cmp_gt_u32_e64 s[46:47], s33, v0
	s_and_b64 s[18:19], s[8:9], s[46:47]
	s_and_saveexec_b64 s[8:9], s[18:19]
	v_lshl_add_u32 v0, v0, 3, s31
	v_add_u32_e32 v4, 0x81, v2
	ds_write_b64 v0, v[4:5]
	s_or_b64 exec, exec, s[8:9]
	s_bcnt1_i32_b64 s8, vcc
	s_bcnt1_i32_b64 s9, s[44:45]
	s_add_i32 s8, s28, s8
	s_add_i32 s28, s8, s9
	s_add_i32 s8, s30, 0x100
	s_cmp_gt_i32 s8, s10
	s_cbranch_scc1 .LBB0_1217
.LBB0_1240:
	v_and_b32_e32 v7, 0xffff, v18
	v_add_u32_e32 v6, 0x100, v2
	v_lshrrev_b32_e32 v5, 16, v18
	v_cmp_gt_u32_e64 s[44:45], s11, v6
	v_cmp_le_u32_e32 vcc, s29, v7
	v_cmp_le_u32_e64 s[46:47], s29, v5
	s_and_b64 s[18:19], s[44:45], vcc
	v_cndmask_b32_e64 v0, 0, 1, s[18:19]
	s_and_b64 s[8:9], s[44:45], s[46:47]
	s_mov_b64 vcc, s[18:19]
	s_mov_b64 s[44:45], s[8:9]
	v_mbcnt_lo_u32_b32 v3, vcc_lo, 0
	v_mbcnt_hi_u32_b32 v3, vcc_hi, v3
	v_mbcnt_lo_u32_b32 v3, s44, v3
	s_min_u32 s26, s28, 0x2c0
	v_mbcnt_hi_u32_b32 v3, s45, v3
	s_sub_i32 s33, 0x2c0, s26
	s_lshl_b32 s27, s26, 3
	v_cmp_gt_u32_e64 s[46:47], s33, v3
	s_add_i32 s31, s88, s27
	s_and_b64 s[18:19], s[18:19], s[46:47]
	s_and_saveexec_b64 s[26:27], s[18:19]
	v_lshl_add_u32 v4, v3, 3, s31
	ds_write_b64 v4, v[6:7]
	s_or_b64 exec, exec, s[26:27]
	v_add_u32_e32 v0, v3, v0
	v_cmp_gt_u32_e64 s[46:47], s33, v0
	s_and_b64 s[18:19], s[8:9], s[46:47]
	s_and_saveexec_b64 s[8:9], s[18:19]
	v_lshl_add_u32 v0, v0, 3, s31
	v_add_u32_e32 v4, 0x101, v2
	ds_write_b64 v0, v[4:5]
	s_or_b64 exec, exec, s[8:9]
	s_bcnt1_i32_b64 s8, vcc
	s_bcnt1_i32_b64 s9, s[44:45]
	s_add_i32 s8, s28, s8
	s_add_i32 s28, s8, s9
	s_add_i32 s8, s30, 0x180
	s_cmp_gt_i32 s8, s10
	s_cbranch_scc1 .LBB0_1218
.LBB0_1245:
	v_and_b32_e32 v7, 0xffff, v19
	v_add_u32_e32 v6, 0x180, v2
	v_lshrrev_b32_e32 v5, 16, v19
	v_cmp_gt_u32_e64 s[44:45], s11, v6
	v_cmp_le_u32_e32 vcc, s29, v7
	v_cmp_le_u32_e64 s[46:47], s29, v5
	s_and_b64 s[18:19], s[44:45], vcc
	v_cndmask_b32_e64 v0, 0, 1, s[18:19]
	s_and_b64 s[8:9], s[44:45], s[46:47]
	s_mov_b64 vcc, s[18:19]
	s_mov_b64 s[44:45], s[8:9]
	v_mbcnt_lo_u32_b32 v3, vcc_lo, 0
	v_mbcnt_hi_u32_b32 v3, vcc_hi, v3
	v_mbcnt_lo_u32_b32 v3, s44, v3
	s_min_u32 s26, s28, 0x2c0
	v_mbcnt_hi_u32_b32 v3, s45, v3
	s_sub_i32 s33, 0x2c0, s26
	s_lshl_b32 s27, s26, 3
	v_cmp_gt_u32_e64 s[46:47], s33, v3
	s_add_i32 s31, s88, s27
	s_and_b64 s[18:19], s[18:19], s[46:47]
	s_and_saveexec_b64 s[26:27], s[18:19]
	v_lshl_add_u32 v4, v3, 3, s31
	ds_write_b64 v4, v[6:7]
	s_or_b64 exec, exec, s[26:27]
	v_add_u32_e32 v0, v3, v0
	v_cmp_gt_u32_e64 s[46:47], s33, v0
	s_and_b64 s[18:19], s[8:9], s[46:47]
	s_and_saveexec_b64 s[8:9], s[18:19]
	v_lshl_add_u32 v0, v0, 3, s31
	v_add_u32_e32 v4, 0x181, v2
	ds_write_b64 v0, v[4:5]
	s_or_b64 exec, exec, s[8:9]
	s_bcnt1_i32_b64 s8, vcc
	s_bcnt1_i32_b64 s9, s[44:45]
	s_add_i32 s8, s28, s8
	s_add_i32 s28, s8, s9
	s_add_i32 s8, s30, 0x200
	s_cmp_gt_i32 s8, s10
	s_cbranch_scc1 .LBB0_1219
.LBB0_1250:
	v_and_b32_e32 v7, 0xffff, v20
	v_add_u32_e32 v6, 0x200, v2
	v_lshrrev_b32_e32 v5, 16, v20
	v_cmp_gt_u32_e64 s[44:45], s11, v6
	v_cmp_le_u32_e32 vcc, s29, v7
	v_cmp_le_u32_e64 s[46:47], s29, v5
	s_and_b64 s[18:19], s[44:45], vcc
	v_cndmask_b32_e64 v0, 0, 1, s[18:19]
	s_and_b64 s[8:9], s[44:45], s[46:47]
	s_mov_b64 vcc, s[18:19]
	s_mov_b64 s[44:45], s[8:9]
	v_mbcnt_lo_u32_b32 v3, vcc_lo, 0
	v_mbcnt_hi_u32_b32 v3, vcc_hi, v3
	v_mbcnt_lo_u32_b32 v3, s44, v3
	s_min_u32 s26, s28, 0x2c0
	v_mbcnt_hi_u32_b32 v3, s45, v3
	s_sub_i32 s33, 0x2c0, s26
	s_lshl_b32 s27, s26, 3
	v_cmp_gt_u32_e64 s[46:47], s33, v3
	s_add_i32 s31, s88, s27
	s_and_b64 s[18:19], s[18:19], s[46:47]
	s_and_saveexec_b64 s[26:27], s[18:19]
	v_lshl_add_u32 v4, v3, 3, s31
	ds_write_b64 v4, v[6:7]
	s_or_b64 exec, exec, s[26:27]
	v_add_u32_e32 v0, v3, v0
	v_cmp_gt_u32_e64 s[46:47], s33, v0
	s_and_b64 s[18:19], s[8:9], s[46:47]
	s_and_saveexec_b64 s[8:9], s[18:19]
	v_lshl_add_u32 v0, v0, 3, s31
	v_add_u32_e32 v4, 0x201, v2
	ds_write_b64 v0, v[4:5]
	s_or_b64 exec, exec, s[8:9]
	s_bcnt1_i32_b64 s8, vcc
	s_bcnt1_i32_b64 s9, s[44:45]
	s_add_i32 s8, s28, s8
	s_add_i32 s28, s8, s9
	s_add_i32 s8, s30, 0x280
	s_cmp_gt_i32 s8, s10
	s_cbranch_scc1 .LBB0_1220
.LBB0_1255:
	v_and_b32_e32 v7, 0xffff, v21
	v_add_u32_e32 v6, 0x280, v2
	v_lshrrev_b32_e32 v5, 16, v21
	v_cmp_gt_u32_e64 s[44:45], s11, v6
	v_cmp_le_u32_e32 vcc, s29, v7
	v_cmp_le_u32_e64 s[46:47], s29, v5
	s_and_b64 s[18:19], s[44:45], vcc
	v_cndmask_b32_e64 v0, 0, 1, s[18:19]
	s_and_b64 s[8:9], s[44:45], s[46:47]
	s_mov_b64 vcc, s[18:19]
	s_mov_b64 s[44:45], s[8:9]
	v_mbcnt_lo_u32_b32 v3, vcc_lo, 0
	v_mbcnt_hi_u32_b32 v3, vcc_hi, v3
	v_mbcnt_lo_u32_b32 v3, s44, v3
	s_min_u32 s26, s28, 0x2c0
	v_mbcnt_hi_u32_b32 v3, s45, v3
	s_sub_i32 s33, 0x2c0, s26
	s_lshl_b32 s27, s26, 3
	v_cmp_gt_u32_e64 s[46:47], s33, v3
	s_add_i32 s31, s88, s27
	s_and_b64 s[18:19], s[18:19], s[46:47]
	s_and_saveexec_b64 s[26:27], s[18:19]
	v_lshl_add_u32 v4, v3, 3, s31
	ds_write_b64 v4, v[6:7]
	s_or_b64 exec, exec, s[26:27]
	v_add_u32_e32 v0, v3, v0
	v_cmp_gt_u32_e64 s[46:47], s33, v0
	s_and_b64 s[18:19], s[8:9], s[46:47]
	s_and_saveexec_b64 s[8:9], s[18:19]
	v_lshl_add_u32 v0, v0, 3, s31
	v_add_u32_e32 v4, 0x281, v2
	ds_write_b64 v0, v[4:5]
	s_or_b64 exec, exec, s[8:9]
	s_bcnt1_i32_b64 s8, vcc
	s_bcnt1_i32_b64 s9, s[44:45]
	s_add_i32 s8, s28, s8
	s_add_i32 s28, s8, s9
	s_add_i32 s8, s30, 0x300
	s_cmp_gt_i32 s8, s10
	s_cbranch_scc1 .LBB0_1221
.LBB0_1260:
	v_and_b32_e32 v7, 0xffff, v22
	v_add_u32_e32 v6, 0x300, v2
	v_lshrrev_b32_e32 v5, 16, v22
	v_cmp_gt_u32_e64 s[44:45], s11, v6
	v_cmp_le_u32_e32 vcc, s29, v7
	v_cmp_le_u32_e64 s[46:47], s29, v5
	s_and_b64 s[18:19], s[44:45], vcc
	v_cndmask_b32_e64 v0, 0, 1, s[18:19]
	s_and_b64 s[8:9], s[44:45], s[46:47]
	s_mov_b64 vcc, s[18:19]
	s_mov_b64 s[44:45], s[8:9]
	v_mbcnt_lo_u32_b32 v3, vcc_lo, 0
	v_mbcnt_hi_u32_b32 v3, vcc_hi, v3
	v_mbcnt_lo_u32_b32 v3, s44, v3
	s_min_u32 s26, s28, 0x2c0
	v_mbcnt_hi_u32_b32 v3, s45, v3
	s_sub_i32 s33, 0x2c0, s26
	s_lshl_b32 s27, s26, 3
	v_cmp_gt_u32_e64 s[46:47], s33, v3
	s_add_i32 s31, s88, s27
	s_and_b64 s[18:19], s[18:19], s[46:47]
	s_and_saveexec_b64 s[26:27], s[18:19]
	v_lshl_add_u32 v4, v3, 3, s31
	ds_write_b64 v4, v[6:7]
	s_or_b64 exec, exec, s[26:27]
	v_add_u32_e32 v0, v3, v0
	v_cmp_gt_u32_e64 s[46:47], s33, v0
	s_and_b64 s[18:19], s[8:9], s[46:47]
	s_and_saveexec_b64 s[8:9], s[18:19]
	v_lshl_add_u32 v0, v0, 3, s31
	v_add_u32_e32 v4, 0x301, v2
	ds_write_b64 v0, v[4:5]
	s_or_b64 exec, exec, s[8:9]
	s_bcnt1_i32_b64 s8, vcc
	s_bcnt1_i32_b64 s9, s[44:45]
	s_add_i32 s8, s28, s8
	s_add_i32 s28, s8, s9
	s_add_i32 s8, s30, 0x380
	s_cmp_gt_i32 s8, s10
	s_cbranch_scc1 .LBB0_1222
.LBB0_1265:
	v_and_b32_e32 v7, 0xffff, v23
	v_add_u32_e32 v6, 0x380, v2
	v_lshrrev_b32_e32 v5, 16, v23
	v_cmp_gt_u32_e64 s[44:45], s11, v6
	v_cmp_le_u32_e32 vcc, s29, v7
	v_cmp_le_u32_e64 s[46:47], s29, v5
	s_and_b64 s[18:19], s[44:45], vcc
	v_cndmask_b32_e64 v0, 0, 1, s[18:19]
	s_and_b64 s[8:9], s[44:45], s[46:47]
	s_mov_b64 vcc, s[18:19]
	s_mov_b64 s[44:45], s[8:9]
	v_mbcnt_lo_u32_b32 v3, vcc_lo, 0
	v_mbcnt_hi_u32_b32 v3, vcc_hi, v3
	v_mbcnt_lo_u32_b32 v3, s44, v3
	s_min_u32 s26, s28, 0x2c0
	v_mbcnt_hi_u32_b32 v3, s45, v3
	s_sub_i32 s33, 0x2c0, s26
	s_lshl_b32 s27, s26, 3
	v_cmp_gt_u32_e64 s[46:47], s33, v3
	s_add_i32 s31, s88, s27
	s_and_b64 s[18:19], s[18:19], s[46:47]
	s_and_saveexec_b64 s[26:27], s[18:19]
	v_lshl_add_u32 v4, v3, 3, s31
	ds_write_b64 v4, v[6:7]
	s_or_b64 exec, exec, s[26:27]
	v_add_u32_e32 v0, v3, v0
	v_cmp_gt_u32_e64 s[46:47], s33, v0
	s_and_b64 s[18:19], s[8:9], s[46:47]
	s_and_saveexec_b64 s[8:9], s[18:19]
	v_lshl_add_u32 v0, v0, 3, s31
	v_add_u32_e32 v4, 0x381, v2
	ds_write_b64 v0, v[4:5]
	s_or_b64 exec, exec, s[8:9]
	s_bcnt1_i32_b64 s8, vcc
	s_bcnt1_i32_b64 s9, s[44:45]
	s_add_i32 s8, s28, s8
	s_add_i32 s28, s8, s9
	s_add_i32 s8, s30, 0x400
	s_cmp_gt_i32 s8, s10
	s_cbranch_scc1 .LBB0_1223
.LBB0_1270:
	v_and_b32_e32 v7, 0xffff, v24
	v_add_u32_e32 v6, 0x400, v2
	v_lshrrev_b32_e32 v5, 16, v24
	v_cmp_gt_u32_e64 s[44:45], s11, v6
	v_cmp_le_u32_e32 vcc, s29, v7
	v_cmp_le_u32_e64 s[46:47], s29, v5
	s_and_b64 s[18:19], s[44:45], vcc
	v_cndmask_b32_e64 v0, 0, 1, s[18:19]
	s_and_b64 s[8:9], s[44:45], s[46:47]
	s_mov_b64 vcc, s[18:19]
	s_mov_b64 s[44:45], s[8:9]
	v_mbcnt_lo_u32_b32 v3, vcc_lo, 0
	v_mbcnt_hi_u32_b32 v3, vcc_hi, v3
	v_mbcnt_lo_u32_b32 v3, s44, v3
	s_min_u32 s26, s28, 0x2c0
	v_mbcnt_hi_u32_b32 v3, s45, v3
	s_sub_i32 s33, 0x2c0, s26
	s_lshl_b32 s27, s26, 3
	v_cmp_gt_u32_e64 s[46:47], s33, v3
	s_add_i32 s31, s88, s27
	s_and_b64 s[18:19], s[18:19], s[46:47]
	s_and_saveexec_b64 s[26:27], s[18:19]
	v_lshl_add_u32 v4, v3, 3, s31
	ds_write_b64 v4, v[6:7]
	s_or_b64 exec, exec, s[26:27]
	v_add_u32_e32 v0, v3, v0
	v_cmp_gt_u32_e64 s[46:47], s33, v0
	s_and_b64 s[18:19], s[8:9], s[46:47]
	s_and_saveexec_b64 s[8:9], s[18:19]
	v_lshl_add_u32 v0, v0, 3, s31
	v_add_u32_e32 v4, 0x401, v2
	ds_write_b64 v0, v[4:5]
	s_or_b64 exec, exec, s[8:9]
	s_bcnt1_i32_b64 s8, vcc
	s_bcnt1_i32_b64 s9, s[44:45]
	s_add_i32 s8, s28, s8
	s_add_i32 s28, s8, s9
	s_add_i32 s8, s30, 0x480
	s_cmp_gt_i32 s8, s10
	s_cbranch_scc1 .LBB0_1224
.LBB0_1275:
	v_and_b32_e32 v7, 0xffff, v25
	v_add_u32_e32 v6, 0x480, v2
	v_lshrrev_b32_e32 v5, 16, v25
	v_cmp_gt_u32_e64 s[44:45], s11, v6
	v_cmp_le_u32_e32 vcc, s29, v7
	v_cmp_le_u32_e64 s[46:47], s29, v5
	s_and_b64 s[18:19], s[44:45], vcc
	v_cndmask_b32_e64 v0, 0, 1, s[18:19]
	s_and_b64 s[8:9], s[44:45], s[46:47]
	s_mov_b64 vcc, s[18:19]
	s_mov_b64 s[44:45], s[8:9]
	v_mbcnt_lo_u32_b32 v3, vcc_lo, 0
	v_mbcnt_hi_u32_b32 v3, vcc_hi, v3
	v_mbcnt_lo_u32_b32 v3, s44, v3
	s_min_u32 s26, s28, 0x2c0
	v_mbcnt_hi_u32_b32 v3, s45, v3
	s_sub_i32 s33, 0x2c0, s26
	s_lshl_b32 s27, s26, 3
	v_cmp_gt_u32_e64 s[46:47], s33, v3
	s_add_i32 s31, s88, s27
	s_and_b64 s[18:19], s[18:19], s[46:47]
	s_and_saveexec_b64 s[26:27], s[18:19]
	v_lshl_add_u32 v4, v3, 3, s31
	ds_write_b64 v4, v[6:7]
	s_or_b64 exec, exec, s[26:27]
	v_add_u32_e32 v0, v3, v0
	v_cmp_gt_u32_e64 s[46:47], s33, v0
	s_and_b64 s[18:19], s[8:9], s[46:47]
	s_and_saveexec_b64 s[8:9], s[18:19]
	v_lshl_add_u32 v0, v0, 3, s31
	v_add_u32_e32 v4, 0x481, v2
	ds_write_b64 v0, v[4:5]
	s_or_b64 exec, exec, s[8:9]
	s_bcnt1_i32_b64 s8, vcc
	s_bcnt1_i32_b64 s9, s[44:45]
	s_add_i32 s8, s28, s8
	s_add_i32 s28, s8, s9
	s_add_i32 s8, s30, 0x500
	s_cmp_gt_i32 s8, s10
	s_cbranch_scc1 .LBB0_1225
.LBB0_1280:
	v_and_b32_e32 v7, 0xffff, v26
	v_add_u32_e32 v6, 0x500, v2
	v_lshrrev_b32_e32 v5, 16, v26
	v_cmp_gt_u32_e64 s[44:45], s11, v6
	v_cmp_le_u32_e32 vcc, s29, v7
	v_cmp_le_u32_e64 s[46:47], s29, v5
	s_and_b64 s[18:19], s[44:45], vcc
	v_cndmask_b32_e64 v0, 0, 1, s[18:19]
	s_and_b64 s[8:9], s[44:45], s[46:47]
	s_mov_b64 vcc, s[18:19]
	s_mov_b64 s[44:45], s[8:9]
	v_mbcnt_lo_u32_b32 v3, vcc_lo, 0
	v_mbcnt_hi_u32_b32 v3, vcc_hi, v3
	v_mbcnt_lo_u32_b32 v3, s44, v3
	s_min_u32 s26, s28, 0x2c0
	v_mbcnt_hi_u32_b32 v3, s45, v3
	s_sub_i32 s33, 0x2c0, s26
	s_lshl_b32 s27, s26, 3
	v_cmp_gt_u32_e64 s[46:47], s33, v3
	s_add_i32 s31, s88, s27
	s_and_b64 s[18:19], s[18:19], s[46:47]
	s_and_saveexec_b64 s[26:27], s[18:19]
	v_lshl_add_u32 v4, v3, 3, s31
	ds_write_b64 v4, v[6:7]
	s_or_b64 exec, exec, s[26:27]
	v_add_u32_e32 v0, v3, v0
	v_cmp_gt_u32_e64 s[46:47], s33, v0
	s_and_b64 s[18:19], s[8:9], s[46:47]
	s_and_saveexec_b64 s[8:9], s[18:19]
	v_lshl_add_u32 v0, v0, 3, s31
	v_add_u32_e32 v4, 0x501, v2
	ds_write_b64 v0, v[4:5]
	s_or_b64 exec, exec, s[8:9]
	s_bcnt1_i32_b64 s8, vcc
	s_bcnt1_i32_b64 s9, s[44:45]
	s_add_i32 s8, s28, s8
	s_add_i32 s28, s8, s9
	s_add_i32 s8, s30, 0x580
	s_cmp_gt_i32 s8, s10
	s_cbranch_scc1 .LBB0_1226
.LBB0_1285:
	v_and_b32_e32 v7, 0xffff, v27
	v_add_u32_e32 v6, 0x580, v2
	v_lshrrev_b32_e32 v5, 16, v27
	v_cmp_gt_u32_e64 s[44:45], s11, v6
	v_cmp_le_u32_e32 vcc, s29, v7
	v_cmp_le_u32_e64 s[46:47], s29, v5
	s_and_b64 s[18:19], s[44:45], vcc
	v_cndmask_b32_e64 v0, 0, 1, s[18:19]
	s_and_b64 s[8:9], s[44:45], s[46:47]
	s_mov_b64 vcc, s[18:19]
	s_mov_b64 s[44:45], s[8:9]
	v_mbcnt_lo_u32_b32 v3, vcc_lo, 0
	v_mbcnt_hi_u32_b32 v3, vcc_hi, v3
	v_mbcnt_lo_u32_b32 v3, s44, v3
	s_min_u32 s26, s28, 0x2c0
	v_mbcnt_hi_u32_b32 v3, s45, v3
	s_sub_i32 s33, 0x2c0, s26
	s_lshl_b32 s27, s26, 3
	v_cmp_gt_u32_e64 s[46:47], s33, v3
	s_add_i32 s31, s88, s27
	s_and_b64 s[18:19], s[18:19], s[46:47]
	s_and_saveexec_b64 s[26:27], s[18:19]
	v_lshl_add_u32 v4, v3, 3, s31
	ds_write_b64 v4, v[6:7]
	s_or_b64 exec, exec, s[26:27]
	v_add_u32_e32 v0, v3, v0
	v_cmp_gt_u32_e64 s[46:47], s33, v0
	s_and_b64 s[18:19], s[8:9], s[46:47]
	s_and_saveexec_b64 s[8:9], s[18:19]
	v_lshl_add_u32 v0, v0, 3, s31
	v_add_u32_e32 v4, 0x581, v2
	ds_write_b64 v0, v[4:5]
	s_or_b64 exec, exec, s[8:9]
	s_bcnt1_i32_b64 s8, vcc
	s_bcnt1_i32_b64 s9, s[44:45]
	s_add_i32 s8, s28, s8
	s_add_i32 s28, s8, s9
	s_add_i32 s8, s30, 0x600
	s_cmp_gt_i32 s8, s10
	s_cbranch_scc1 .LBB0_1227
.LBB0_1290:
	v_and_b32_e32 v7, 0xffff, v28
	v_add_u32_e32 v6, 0x600, v2
	v_lshrrev_b32_e32 v5, 16, v28
	v_cmp_gt_u32_e64 s[44:45], s11, v6
	v_cmp_le_u32_e32 vcc, s29, v7
	v_cmp_le_u32_e64 s[46:47], s29, v5
	s_and_b64 s[18:19], s[44:45], vcc
	v_cndmask_b32_e64 v0, 0, 1, s[18:19]
	s_and_b64 s[8:9], s[44:45], s[46:47]
	s_mov_b64 vcc, s[18:19]
	s_mov_b64 s[44:45], s[8:9]
	v_mbcnt_lo_u32_b32 v3, vcc_lo, 0
	v_mbcnt_hi_u32_b32 v3, vcc_hi, v3
	v_mbcnt_lo_u32_b32 v3, s44, v3
	s_min_u32 s26, s28, 0x2c0
	v_mbcnt_hi_u32_b32 v3, s45, v3
	s_sub_i32 s33, 0x2c0, s26
	s_lshl_b32 s27, s26, 3
	v_cmp_gt_u32_e64 s[46:47], s33, v3
	s_add_i32 s31, s88, s27
	s_and_b64 s[18:19], s[18:19], s[46:47]
	s_and_saveexec_b64 s[26:27], s[18:19]
	v_lshl_add_u32 v4, v3, 3, s31
	ds_write_b64 v4, v[6:7]
	s_or_b64 exec, exec, s[26:27]
	v_add_u32_e32 v0, v3, v0
	v_cmp_gt_u32_e64 s[46:47], s33, v0
	s_and_b64 s[18:19], s[8:9], s[46:47]
	s_and_saveexec_b64 s[8:9], s[18:19]
	v_lshl_add_u32 v0, v0, 3, s31
	v_add_u32_e32 v4, 0x601, v2
	ds_write_b64 v0, v[4:5]
	s_or_b64 exec, exec, s[8:9]
	s_bcnt1_i32_b64 s8, vcc
	s_bcnt1_i32_b64 s9, s[44:45]
	s_add_i32 s8, s28, s8
	s_add_i32 s28, s8, s9
	s_add_i32 s8, s30, 0x680
	s_cmp_gt_i32 s8, s10
	s_cbranch_scc1 .LBB0_1228
.LBB0_1295:
	v_and_b32_e32 v7, 0xffff, v29
	v_add_u32_e32 v6, 0x680, v2
	v_lshrrev_b32_e32 v5, 16, v29
	v_cmp_gt_u32_e64 s[44:45], s11, v6
	v_cmp_le_u32_e32 vcc, s29, v7
	v_cmp_le_u32_e64 s[46:47], s29, v5
	s_and_b64 s[18:19], s[44:45], vcc
	v_cndmask_b32_e64 v0, 0, 1, s[18:19]
	s_and_b64 s[8:9], s[44:45], s[46:47]
	s_mov_b64 vcc, s[18:19]
	s_mov_b64 s[44:45], s[8:9]
	v_mbcnt_lo_u32_b32 v3, vcc_lo, 0
	v_mbcnt_hi_u32_b32 v3, vcc_hi, v3
	v_mbcnt_lo_u32_b32 v3, s44, v3
	s_min_u32 s26, s28, 0x2c0
	v_mbcnt_hi_u32_b32 v3, s45, v3
	s_sub_i32 s33, 0x2c0, s26
	s_lshl_b32 s27, s26, 3
	v_cmp_gt_u32_e64 s[46:47], s33, v3
	s_add_i32 s31, s88, s27
	s_and_b64 s[18:19], s[18:19], s[46:47]
	s_and_saveexec_b64 s[26:27], s[18:19]
	v_lshl_add_u32 v4, v3, 3, s31
	ds_write_b64 v4, v[6:7]
	s_or_b64 exec, exec, s[26:27]
	v_add_u32_e32 v0, v3, v0
	v_cmp_gt_u32_e64 s[46:47], s33, v0
	s_and_b64 s[18:19], s[8:9], s[46:47]
	s_and_saveexec_b64 s[8:9], s[18:19]
	v_lshl_add_u32 v0, v0, 3, s31
	v_add_u32_e32 v4, 0x681, v2
	ds_write_b64 v0, v[4:5]
	s_or_b64 exec, exec, s[8:9]
	s_bcnt1_i32_b64 s8, vcc
	s_bcnt1_i32_b64 s9, s[44:45]
	s_add_i32 s8, s28, s8
	s_add_i32 s28, s8, s9
	s_add_i32 s8, s30, 0x700
	s_cmp_gt_i32 s8, s10
	s_cbranch_scc1 .LBB0_1229
.LBB0_1300:
	v_and_b32_e32 v7, 0xffff, v30
	v_add_u32_e32 v6, 0x700, v2
	v_lshrrev_b32_e32 v5, 16, v30
	v_cmp_gt_u32_e64 s[44:45], s11, v6
	v_cmp_le_u32_e32 vcc, s29, v7
	v_cmp_le_u32_e64 s[46:47], s29, v5
	s_and_b64 s[18:19], s[44:45], vcc
	v_cndmask_b32_e64 v0, 0, 1, s[18:19]
	s_and_b64 s[8:9], s[44:45], s[46:47]
	s_mov_b64 vcc, s[18:19]
	s_mov_b64 s[44:45], s[8:9]
	v_mbcnt_lo_u32_b32 v3, vcc_lo, 0
	v_mbcnt_hi_u32_b32 v3, vcc_hi, v3
	v_mbcnt_lo_u32_b32 v3, s44, v3
	s_min_u32 s26, s28, 0x2c0
	v_mbcnt_hi_u32_b32 v3, s45, v3
	s_sub_i32 s33, 0x2c0, s26
	s_lshl_b32 s27, s26, 3
	v_cmp_gt_u32_e64 s[46:47], s33, v3
	s_add_i32 s31, s88, s27
	s_and_b64 s[18:19], s[18:19], s[46:47]
	s_and_saveexec_b64 s[26:27], s[18:19]
	v_lshl_add_u32 v4, v3, 3, s31
	ds_write_b64 v4, v[6:7]
	s_or_b64 exec, exec, s[26:27]
	v_add_u32_e32 v0, v3, v0
	v_cmp_gt_u32_e64 s[46:47], s33, v0
	s_and_b64 s[18:19], s[8:9], s[46:47]
	s_and_saveexec_b64 s[8:9], s[18:19]
	v_lshl_add_u32 v0, v0, 3, s31
	v_add_u32_e32 v4, 0x701, v2
	ds_write_b64 v0, v[4:5]
	s_or_b64 exec, exec, s[8:9]
	s_bcnt1_i32_b64 s8, vcc
	s_bcnt1_i32_b64 s9, s[44:45]
	s_add_i32 s8, s28, s8
	s_add_i32 s28, s8, s9
	s_add_i32 s8, s30, 0x780
	s_cmp_gt_i32 s8, s10
	s_cbranch_scc1 .LBB0_1310
.LBB0_1305:
	v_and_b32_e32 v5, 0xffff, v31
	v_add_u32_e32 v4, 0x780, v2
	v_lshrrev_b32_e32 v3, 16, v31
	v_cmp_gt_u32_e64 s[44:45], s11, v4
	v_cmp_le_u32_e32 vcc, s29, v5
	v_cmp_le_u32_e64 s[46:47], s29, v3
	s_and_b64 s[18:19], s[44:45], vcc
	v_cndmask_b32_e64 v0, 0, 1, s[18:19]
	s_and_b64 s[8:9], s[44:45], s[46:47]
	s_mov_b64 vcc, s[18:19]
	s_mov_b64 s[44:45], s[8:9]
	v_mbcnt_lo_u32_b32 v6, vcc_lo, 0
	v_mbcnt_hi_u32_b32 v6, vcc_hi, v6
	v_mbcnt_lo_u32_b32 v6, s44, v6
	s_min_u32 s26, s28, 0x2c0
	v_mbcnt_hi_u32_b32 v6, s45, v6
	s_sub_i32 s31, 0x2c0, s26
	s_lshl_b32 s27, s26, 3
	v_cmp_gt_u32_e64 s[46:47], s31, v6
	s_add_i32 s30, s88, s27
	s_and_b64 s[18:19], s[18:19], s[46:47]
	s_and_saveexec_b64 s[26:27], s[18:19]
	v_lshl_add_u32 v7, v6, 3, s30
	ds_write_b64 v7, v[4:5]
	s_or_b64 exec, exec, s[26:27]
	v_add_u32_e32 v0, v6, v0
	v_cmp_gt_u32_e64 s[46:47], s31, v0
	s_and_b64 s[18:19], s[8:9], s[46:47]
	s_and_saveexec_b64 s[8:9], s[18:19]
	v_lshl_add_u32 v0, v0, 3, s30
	v_add_u32_e32 v2, 0x781, v2
	ds_write_b64 v0, v[2:3]
	s_or_b64 exec, exec, s[8:9]
	s_bcnt1_i32_b64 s8, vcc
	s_bcnt1_i32_b64 s9, s[44:45]
	s_add_i32 s8, s28, s8
	s_add_i32 s28, s8, s9

.LBB0_1380:
	v_cmp_eq_u32_e32 vcc, v55, v5
	v_cmp_gt_u32_e64 s[44:45], v55, v5
	s_nop 0
	v_mbcnt_lo_u32_b32 v55, vcc_lo, 0
	v_mbcnt_hi_u32_b32 v55, vcc_hi, v55
	v_cmp_gt_u32_e64 s[46:47], s4, v55
	s_and_b64 s[6:7], vcc, s[46:47]
	s_or_b64 s[6:7], s[44:45], s[6:7]
	s_mov_b64 s[44:45], s[6:7]
	s_nop 1
	v_mbcnt_lo_u32_b32 v55, s44, 0
	v_mbcnt_hi_u32_b32 v55, s45, v55
	v_cmp_gt_u32_e64 s[46:47], s75, v55
	s_and_b64 s[8:9], s[6:7], s[46:47]
	s_and_saveexec_b64 s[6:7], s[8:9]
	v_lshl_add_u32 v55, v55, 2, s74
	ds_write_b32 v55, v54
	s_or_b64 exec, exec, s[6:7]
	s_bcnt1_i32_b64 s9, vcc
	v_cmp_eq_u32_e32 vcc, v53, v5
	s_bcnt1_i32_b64 s8, s[44:45]
	v_cmp_gt_u32_e64 s[44:45], v53, v5
	v_mbcnt_lo_u32_b32 v53, vcc_lo, 0
	v_mbcnt_hi_u32_b32 v53, vcc_hi, v53
	v_add_u32_e32 v53, s9, v53
	v_cmp_gt_u32_e64 s[46:47], s4, v53
	s_and_b64 s[6:7], vcc, s[46:47]
	s_or_b64 s[6:7], s[44:45], s[6:7]
	s_mov_b64 s[44:45], s[6:7]
	s_nop 1
	v_mbcnt_lo_u32_b32 v53, s44, 0
	v_mbcnt_hi_u32_b32 v53, s45, v53
	v_add_u32_e32 v53, s8, v53
	v_cmp_gt_u32_e64 s[46:47], s75, v53
	s_and_b64 s[18:19], s[6:7], s[46:47]
	s_and_saveexec_b64 s[6:7], s[18:19]
	v_lshl_add_u32 v53, v53, 2, s74
	ds_write_b32 v53, v52
	s_or_b64 exec, exec, s[6:7]
	s_bcnt1_i32_b64 s6, s[44:45]
	s_add_i32 s8, s6, s8
	s_bcnt1_i32_b64 s6, vcc
	v_cmp_eq_u32_e32 vcc, v51, v5
	v_cmp_gt_u32_e64 s[44:45], v51, v5
	s_add_i32 s9, s6, s9
	v_mbcnt_lo_u32_b32 v51, vcc_lo, 0
	v_mbcnt_hi_u32_b32 v51, vcc_hi, v51
	v_add_u32_e32 v51, s9, v51
	v_cmp_gt_u32_e64 s[46:47], s4, v51
	s_and_b64 s[6:7], vcc, s[46:47]
	s_or_b64 s[6:7], s[44:45], s[6:7]
	s_mov_b64 s[44:45], s[6:7]
	s_nop 1
	v_mbcnt_lo_u32_b32 v51, s44, 0
	v_mbcnt_hi_u32_b32 v51, s45, v51
	v_add_u32_e32 v51, s8, v51
	v_cmp_gt_u32_e64 s[46:47], s75, v51
	s_and_b64 s[18:19], s[6:7], s[46:47]
	s_and_saveexec_b64 s[6:7], s[18:19]
	v_lshl_add_u32 v51, v51, 2, s74
	ds_write_b32 v51, v50
	s_or_b64 exec, exec, s[6:7]
	s_bcnt1_i32_b64 s6, s[44:45]
	s_add_i32 s8, s8, s6
	s_bcnt1_i32_b64 s6, vcc
	v_cmp_eq_u32_e32 vcc, v49, v5
	v_cmp_gt_u32_e64 s[44:45], v49, v5
	s_add_i32 s9, s9, s6
	v_mbcnt_lo_u32_b32 v49, vcc_lo, 0
	v_mbcnt_hi_u32_b32 v49, vcc_hi, v49
	v_add_u32_e32 v49, s9, v49
	v_cmp_gt_u32_e64 s[46:47], s4, v49
	s_and_b64 s[6:7], vcc, s[46:47]
	s_or_b64 s[6:7], s[44:45], s[6:7]
	s_mov_b64 s[44:45], s[6:7]
	s_nop 1
	v_mbcnt_lo_u32_b32 v49, s44, 0
	v_mbcnt_hi_u32_b32 v49, s45, v49
	v_add_u32_e32 v49, s8, v49
	v_cmp_gt_u32_e64 s[46:47], s75, v49
	s_and_b64 s[18:19], s[6:7], s[46:47]
	s_and_saveexec_b64 s[6:7], s[18:19]
	v_lshl_add_u32 v49, v49, 2, s74
	ds_write_b32 v49, v48
	s_or_b64 exec, exec, s[6:7]
	s_bcnt1_i32_b64 s6, s[44:45]
	s_add_i32 s8, s8, s6
	s_bcnt1_i32_b64 s6, vcc
	v_cmp_eq_u32_e32 vcc, v15, v5
	v_cmp_gt_u32_e64 s[44:45], v15, v5
	s_add_i32 s9, s9, s6
	v_mbcnt_lo_u32_b32 v15, vcc_lo, 0
	v_mbcnt_hi_u32_b32 v15, vcc_hi, v15
	v_add_u32_e32 v15, s9, v15
	v_cmp_gt_u32_e64 s[46:47], s4, v15
	s_and_b64 s[6:7], vcc, s[46:47]
	s_or_b64 s[6:7], s[44:45], s[6:7]
	s_mov_b64 s[44:45], s[6:7]
	s_nop 1
	v_mbcnt_lo_u32_b32 v15, s44, 0
	v_mbcnt_hi_u32_b32 v15, s45, v15
	v_add_u32_e32 v15, s8, v15
	v_cmp_gt_u32_e64 s[46:47], s75, v15
	s_and_b64 s[18:19], s[6:7], s[46:47]
	s_and_saveexec_b64 s[6:7], s[18:19]
	v_lshl_add_u32 v15, v15, 2, s74
	ds_write_b32 v15, v14
	s_or_b64 exec, exec, s[6:7]
	s_bcnt1_i32_b64 s6, s[44:45]
	s_add_i32 s8, s8, s6
	s_bcnt1_i32_b64 s6, vcc
	v_cmp_eq_u32_e32 vcc, v13, v5
	v_cmp_gt_u32_e64 s[44:45], v13, v5
	s_add_i32 s9, s9, s6
	v_mbcnt_lo_u32_b32 v13, vcc_lo, 0
	v_mbcnt_hi_u32_b32 v13, vcc_hi, v13
	v_add_u32_e32 v13, s9, v13
	v_cmp_gt_u32_e64 s[46:47], s4, v13
	s_and_b64 s[6:7], vcc, s[46:47]
	s_or_b64 s[6:7], s[44:45], s[6:7]
	s_mov_b64 s[44:45], s[6:7]
	s_nop 1
	v_mbcnt_lo_u32_b32 v13, s44, 0
	v_mbcnt_hi_u32_b32 v13, s45, v13
	v_add_u32_e32 v13, s8, v13
	v_cmp_gt_u32_e64 s[46:47], s75, v13
	s_and_b64 s[18:19], s[6:7], s[46:47]
	s_and_saveexec_b64 s[6:7], s[18:19]
	v_lshl_add_u32 v13, v13, 2, s74
	ds_write_b32 v13, v12
	s_or_b64 exec, exec, s[6:7]
	s_bcnt1_i32_b64 s6, s[44:45]
	s_add_i32 s8, s8, s6
	s_bcnt1_i32_b64 s6, vcc
	v_cmp_eq_u32_e32 vcc, v11, v5
	v_cmp_gt_u32_e64 s[44:45], v11, v5
	s_add_i32 s9, s9, s6
	v_mbcnt_lo_u32_b32 v11, vcc_lo, 0
	v_mbcnt_hi_u32_b32 v11, vcc_hi, v11
	v_add_u32_e32 v11, s9, v11
	v_cmp_gt_u32_e64 s[46:47], s4, v11
	s_and_b64 s[6:7], vcc, s[46:47]
	s_or_b64 s[6:7], s[44:45], s[6:7]
	s_mov_b64 s[44:45], s[6:7]
	s_nop 1
	v_mbcnt_lo_u32_b32 v11, s44, 0
	v_mbcnt_hi_u32_b32 v11, s45, v11
	v_add_u32_e32 v11, s8, v11
	v_cmp_gt_u32_e64 s[46:47], s75, v11
	s_and_b64 s[18:19], s[6:7], s[46:47]
	s_and_saveexec_b64 s[6:7], s[18:19]
	v_lshl_add_u32 v11, v11, 2, s74
	ds_write_b32 v11, v10
	s_or_b64 exec, exec, s[6:7]
	s_bcnt1_i32_b64 s6, s[44:45]
	s_add_i32 s8, s8, s6
	s_bcnt1_i32_b64 s6, vcc
	v_cmp_eq_u32_e32 vcc, v9, v5
	v_cmp_gt_u32_e64 s[44:45], v9, v5
	s_add_i32 s9, s9, s6
	v_mbcnt_lo_u32_b32 v9, vcc_lo, 0
	v_mbcnt_hi_u32_b32 v9, vcc_hi, v9
	v_add_u32_e32 v9, s9, v9
	v_cmp_gt_u32_e64 s[46:47], s4, v9
	s_and_b64 s[6:7], vcc, s[46:47]
	s_or_b64 s[6:7], s[44:45], s[6:7]
	s_mov_b64 s[44:45], s[6:7]
	s_nop 1
	v_mbcnt_lo_u32_b32 v9, s44, 0
	v_mbcnt_hi_u32_b32 v9, s45, v9
	v_add_u32_e32 v9, s8, v9
	v_cmp_gt_u32_e64 s[46:47], s75, v9
	s_and_b64 s[18:19], s[6:7], s[46:47]
	s_and_saveexec_b64 s[6:7], s[18:19]
	v_lshl_add_u32 v9, v9, 2, s74
	ds_write_b32 v9, v8
	s_or_b64 exec, exec, s[6:7]
	s_bcnt1_i32_b64 s6, s[44:45]
	s_add_i32 s8, s8, s6
	s_bcnt1_i32_b64 s6, vcc
	v_cmp_eq_u32_e32 vcc, v7, v5
	v_cmp_gt_u32_e64 s[44:45], v7, v5
	s_add_i32 s9, s9, s6
	v_mbcnt_lo_u32_b32 v7, vcc_lo, 0
	v_mbcnt_hi_u32_b32 v7, vcc_hi, v7
	v_add_u32_e32 v7, s9, v7
	v_cmp_gt_u32_e64 s[46:47], s4, v7
	s_and_b64 s[6:7], vcc, s[46:47]
	s_or_b64 s[6:7], s[44:45], s[6:7]
	s_mov_b64 s[44:45], s[6:7]
	s_nop 1
	v_mbcnt_lo_u32_b32 v7, s44, 0
	v_mbcnt_hi_u32_b32 v7, s45, v7
	v_add_u32_e32 v7, s8, v7
	v_cmp_gt_u32_e64 s[46:47], s75, v7
	s_and_b64 s[18:19], s[6:7], s[46:47]
	s_and_saveexec_b64 s[6:7], s[18:19]
	v_lshl_add_u32 v7, v7, 2, s74
	ds_write_b32 v7, v6
	s_or_b64 exec, exec, s[6:7]
	s_bcnt1_i32_b64 s6, s[44:45]
	s_add_i32 s8, s8, s6
	s_bcnt1_i32_b64 s6, vcc
	v_cmp_eq_u32_e32 vcc, v0, v5
	v_cmp_gt_u32_e64 s[44:45], v0, v5
	s_add_i32 s9, s9, s6
	v_mbcnt_lo_u32_b32 v0, vcc_lo, 0
	v_mbcnt_hi_u32_b32 v0, vcc_hi, v0
	v_add_u32_e32 v0, s9, v0
	v_cmp_gt_u32_e64 s[46:47], s4, v0
	s_and_b64 s[6:7], vcc, s[46:47]
	s_or_b64 s[6:7], s[44:45], s[6:7]
	s_mov_b64 s[44:45], s[6:7]
	s_nop 1
	v_mbcnt_lo_u32_b32 v0, s44, 0
	v_mbcnt_hi_u32_b32 v0, s45, v0
	v_add_u32_e32 v0, s8, v0
	v_cmp_gt_u32_e64 s[46:47], s75, v0
	s_and_b64 s[18:19], s[6:7], s[46:47]
	s_and_saveexec_b64 s[6:7], s[18:19]
	v_lshl_add_u32 v0, v0, 2, s74
	ds_write_b32 v0, v4
	s_or_b64 exec, exec, s[6:7]
	s_bcnt1_i32_b64 s6, s[44:45]
	v_cmp_eq_u32_e64 s[44:45], v3, v5
	s_add_i32 s8, s8, s6
	s_bcnt1_i32_b64 s6, vcc
	v_mbcnt_lo_u32_b32 v0, s44, 0
	s_add_i32 s9, s9, s6
	v_mbcnt_hi_u32_b32 v0, s45, v0
	v_add_u32_e32 v0, s9, v0
	v_cmp_gt_u32_e64 s[46:47], s4, v0
	v_cmp_gt_u32_e32 vcc, v3, v5
	s_and_b64 s[6:7], s[44:45], s[46:47]
	s_or_b64 s[6:7], vcc, s[6:7]
	s_mov_b64 vcc, s[6:7]
	s_nop 1
	v_mbcnt_lo_u32_b32 v0, vcc_lo, 0
	v_mbcnt_hi_u32_b32 v0, vcc_hi, v0
	v_add_u32_e32 v0, s8, v0
	v_cmp_gt_u32_e32 vcc, s75, v0
	s_and_b64 s[8:9], s[6:7], vcc
	s_and_saveexec_b64 s[6:7], s[8:9]
	v_lshl_add_u32 v0, v0, 2, s74
	ds_write_b32 v0, v2
	s_or_b64 exec, exec, s[6:7]

.LBB0_1414:
	v_cmp_eq_u32_e32 vcc, v55, v5
	v_cmp_gt_u32_e64 s[44:45], v55, v5
	s_nop 0
	v_mbcnt_lo_u32_b32 v55, vcc_lo, 0
	v_mbcnt_hi_u32_b32 v55, vcc_hi, v55
	v_cmp_gt_u32_e64 s[46:47], s4, v55
	s_and_b64 s[6:7], vcc, s[46:47]
	s_or_b64 s[6:7], s[44:45], s[6:7]
	s_mov_b64 s[44:45], s[6:7]
	s_nop 1
	v_mbcnt_lo_u32_b32 v55, s44, 0
	v_mbcnt_hi_u32_b32 v55, s45, v55
	v_cmp_gt_u32_e64 s[46:47], s75, v55
	s_and_b64 s[8:9], s[6:7], s[46:47]
	s_and_saveexec_b64 s[6:7], s[8:9]
	v_lshl_add_u32 v55, v55, 2, s95
	ds_write_b32 v55, v54
	s_or_b64 exec, exec, s[6:7]
	s_bcnt1_i32_b64 s9, vcc
	v_cmp_eq_u32_e32 vcc, v53, v5
	s_bcnt1_i32_b64 s8, s[44:45]
	v_cmp_gt_u32_e64 s[44:45], v53, v5
	v_mbcnt_lo_u32_b32 v53, vcc_lo, 0
	v_mbcnt_hi_u32_b32 v53, vcc_hi, v53
	v_add_u32_e32 v53, s9, v53
	v_cmp_gt_u32_e64 s[46:47], s4, v53
	s_and_b64 s[6:7], vcc, s[46:47]
	s_or_b64 s[6:7], s[44:45], s[6:7]
	s_mov_b64 s[44:45], s[6:7]
	s_nop 1
	v_mbcnt_lo_u32_b32 v53, s44, 0
	v_mbcnt_hi_u32_b32 v53, s45, v53
	v_add_u32_e32 v53, s8, v53
	v_cmp_gt_u32_e64 s[46:47], s75, v53
	s_and_b64 s[18:19], s[6:7], s[46:47]
	s_and_saveexec_b64 s[6:7], s[18:19]
	v_lshl_add_u32 v53, v53, 2, s95
	ds_write_b32 v53, v52
	s_or_b64 exec, exec, s[6:7]
	s_bcnt1_i32_b64 s6, s[44:45]
	s_add_i32 s8, s6, s8
	s_bcnt1_i32_b64 s6, vcc
	v_cmp_eq_u32_e32 vcc, v51, v5
	v_cmp_gt_u32_e64 s[44:45], v51, v5
	s_add_i32 s9, s6, s9
	v_mbcnt_lo_u32_b32 v51, vcc_lo, 0
	v_mbcnt_hi_u32_b32 v51, vcc_hi, v51
	v_add_u32_e32 v51, s9, v51
	v_cmp_gt_u32_e64 s[46:47], s4, v51
	s_and_b64 s[6:7], vcc, s[46:47]
	s_or_b64 s[6:7], s[44:45], s[6:7]
	s_mov_b64 s[44:45], s[6:7]
	s_nop 1
	v_mbcnt_lo_u32_b32 v51, s44, 0
	v_mbcnt_hi_u32_b32 v51, s45, v51
	v_add_u32_e32 v51, s8, v51
	v_cmp_gt_u32_e64 s[46:47], s75, v51
	s_and_b64 s[18:19], s[6:7], s[46:47]
	s_and_saveexec_b64 s[6:7], s[18:19]
	v_lshl_add_u32 v51, v51, 2, s95
	ds_write_b32 v51, v50
	s_or_b64 exec, exec, s[6:7]
	s_bcnt1_i32_b64 s6, s[44:45]
	s_add_i32 s8, s8, s6
	s_bcnt1_i32_b64 s6, vcc
	v_cmp_eq_u32_e32 vcc, v49, v5
	v_cmp_gt_u32_e64 s[44:45], v49, v5
	s_add_i32 s9, s9, s6
	v_mbcnt_lo_u32_b32 v49, vcc_lo, 0
	v_mbcnt_hi_u32_b32 v49, vcc_hi, v49
	v_add_u32_e32 v49, s9, v49
	v_cmp_gt_u32_e64 s[46:47], s4, v49
	s_and_b64 s[6:7], vcc, s[46:47]
	s_or_b64 s[6:7], s[44:45], s[6:7]
	s_mov_b64 s[44:45], s[6:7]
	s_nop 1
	v_mbcnt_lo_u32_b32 v49, s44, 0
	v_mbcnt_hi_u32_b32 v49, s45, v49
	v_add_u32_e32 v49, s8, v49
	v_cmp_gt_u32_e64 s[46:47], s75, v49
	s_and_b64 s[18:19], s[6:7], s[46:47]
	s_and_saveexec_b64 s[6:7], s[18:19]
	v_lshl_add_u32 v49, v49, 2, s95
	ds_write_b32 v49, v48
	s_or_b64 exec, exec, s[6:7]
	s_bcnt1_i32_b64 s6, s[44:45]
	s_add_i32 s8, s8, s6
	s_bcnt1_i32_b64 s6, vcc
	v_cmp_eq_u32_e32 vcc, v15, v5
	v_cmp_gt_u32_e64 s[44:45], v15, v5
	s_add_i32 s9, s9, s6
	v_mbcnt_lo_u32_b32 v15, vcc_lo, 0
	v_mbcnt_hi_u32_b32 v15, vcc_hi, v15
	v_add_u32_e32 v15, s9, v15
	v_cmp_gt_u32_e64 s[46:47], s4, v15
	s_and_b64 s[6:7], vcc, s[46:47]
	s_or_b64 s[6:7], s[44:45], s[6:7]
	s_mov_b64 s[44:45], s[6:7]
	s_nop 1
	v_mbcnt_lo_u32_b32 v15, s44, 0
	v_mbcnt_hi_u32_b32 v15, s45, v15
	v_add_u32_e32 v15, s8, v15
	v_cmp_gt_u32_e64 s[46:47], s75, v15
	s_and_b64 s[18:19], s[6:7], s[46:47]
	s_and_saveexec_b64 s[6:7], s[18:19]
	v_lshl_add_u32 v15, v15, 2, s95
	ds_write_b32 v15, v14
	s_or_b64 exec, exec, s[6:7]
	s_bcnt1_i32_b64 s6, s[44:45]
	s_add_i32 s8, s8, s6
	s_bcnt1_i32_b64 s6, vcc
	v_cmp_eq_u32_e32 vcc, v13, v5
	v_cmp_gt_u32_e64 s[44:45], v13, v5
	s_add_i32 s9, s9, s6
	v_mbcnt_lo_u32_b32 v13, vcc_lo, 0
	v_mbcnt_hi_u32_b32 v13, vcc_hi, v13
	v_add_u32_e32 v13, s9, v13
	v_cmp_gt_u32_e64 s[46:47], s4, v13
	s_and_b64 s[6:7], vcc, s[46:47]
	s_or_b64 s[6:7], s[44:45], s[6:7]
	s_mov_b64 s[44:45], s[6:7]
	s_nop 1
	v_mbcnt_lo_u32_b32 v13, s44, 0
	v_mbcnt_hi_u32_b32 v13, s45, v13
	v_add_u32_e32 v13, s8, v13
	v_cmp_gt_u32_e64 s[46:47], s75, v13
	s_and_b64 s[18:19], s[6:7], s[46:47]
	s_and_saveexec_b64 s[6:7], s[18:19]
	v_lshl_add_u32 v13, v13, 2, s95
	ds_write_b32 v13, v12
	s_or_b64 exec, exec, s[6:7]
	s_bcnt1_i32_b64 s6, s[44:45]
	s_add_i32 s8, s8, s6
	s_bcnt1_i32_b64 s6, vcc
	v_cmp_eq_u32_e32 vcc, v11, v5
	v_cmp_gt_u32_e64 s[44:45], v11, v5
	s_add_i32 s9, s9, s6
	v_mbcnt_lo_u32_b32 v11, vcc_lo, 0
	v_mbcnt_hi_u32_b32 v11, vcc_hi, v11
	v_add_u32_e32 v11, s9, v11
	v_cmp_gt_u32_e64 s[46:47], s4, v11
	s_and_b64 s[6:7], vcc, s[46:47]
	s_or_b64 s[6:7], s[44:45], s[6:7]
	s_mov_b64 s[44:45], s[6:7]
	s_nop 1
	v_mbcnt_lo_u32_b32 v11, s44, 0
	v_mbcnt_hi_u32_b32 v11, s45, v11
	v_add_u32_e32 v11, s8, v11
	v_cmp_gt_u32_e64 s[46:47], s75, v11
	s_and_b64 s[18:19], s[6:7], s[46:47]
	s_and_saveexec_b64 s[6:7], s[18:19]
	v_lshl_add_u32 v11, v11, 2, s95
	ds_write_b32 v11, v10
	s_or_b64 exec, exec, s[6:7]
	s_bcnt1_i32_b64 s6, s[44:45]
	s_add_i32 s8, s8, s6
	s_bcnt1_i32_b64 s6, vcc
	v_cmp_eq_u32_e32 vcc, v9, v5
	v_cmp_gt_u32_e64 s[44:45], v9, v5
	s_add_i32 s9, s9, s6
	v_mbcnt_lo_u32_b32 v9, vcc_lo, 0
	v_mbcnt_hi_u32_b32 v9, vcc_hi, v9
	v_add_u32_e32 v9, s9, v9
	v_cmp_gt_u32_e64 s[46:47], s4, v9
	s_and_b64 s[6:7], vcc, s[46:47]
	s_or_b64 s[6:7], s[44:45], s[6:7]
	s_mov_b64 s[44:45], s[6:7]
	s_nop 1
	v_mbcnt_lo_u32_b32 v9, s44, 0
	v_mbcnt_hi_u32_b32 v9, s45, v9
	v_add_u32_e32 v9, s8, v9
	v_cmp_gt_u32_e64 s[46:47], s75, v9
	s_and_b64 s[18:19], s[6:7], s[46:47]
	s_and_saveexec_b64 s[6:7], s[18:19]
	v_lshl_add_u32 v9, v9, 2, s95
	ds_write_b32 v9, v8
	s_or_b64 exec, exec, s[6:7]
	s_bcnt1_i32_b64 s6, s[44:45]
	s_add_i32 s8, s8, s6
	s_bcnt1_i32_b64 s6, vcc
	v_cmp_eq_u32_e32 vcc, v7, v5
	v_cmp_gt_u32_e64 s[44:45], v7, v5
	s_add_i32 s9, s9, s6
	v_mbcnt_lo_u32_b32 v7, vcc_lo, 0
	v_mbcnt_hi_u32_b32 v7, vcc_hi, v7
	v_add_u32_e32 v7, s9, v7
	v_cmp_gt_u32_e64 s[46:47], s4, v7
	s_and_b64 s[6:7], vcc, s[46:47]
	s_or_b64 s[6:7], s[44:45], s[6:7]
	s_mov_b64 s[44:45], s[6:7]
	s_nop 1
	v_mbcnt_lo_u32_b32 v7, s44, 0
	v_mbcnt_hi_u32_b32 v7, s45, v7
	v_add_u32_e32 v7, s8, v7
	v_cmp_gt_u32_e64 s[46:47], s75, v7
	s_and_b64 s[18:19], s[6:7], s[46:47]
	s_and_saveexec_b64 s[6:7], s[18:19]
	v_lshl_add_u32 v7, v7, 2, s95
	ds_write_b32 v7, v6
	s_or_b64 exec, exec, s[6:7]
	s_bcnt1_i32_b64 s6, s[44:45]
	s_add_i32 s8, s8, s6
	s_bcnt1_i32_b64 s6, vcc
	v_cmp_eq_u32_e32 vcc, v0, v5
	v_cmp_gt_u32_e64 s[44:45], v0, v5
	s_add_i32 s9, s9, s6
	v_mbcnt_lo_u32_b32 v0, vcc_lo, 0
	v_mbcnt_hi_u32_b32 v0, vcc_hi, v0
	v_add_u32_e32 v0, s9, v0
	v_cmp_gt_u32_e64 s[46:47], s4, v0
	s_and_b64 s[6:7], vcc, s[46:47]
	s_or_b64 s[6:7], s[44:45], s[6:7]
	s_mov_b64 s[44:45], s[6:7]
	s_nop 1
	v_mbcnt_lo_u32_b32 v0, s44, 0
	v_mbcnt_hi_u32_b32 v0, s45, v0
	v_add_u32_e32 v0, s8, v0
	v_cmp_gt_u32_e64 s[46:47], s75, v0
	s_and_b64 s[18:19], s[6:7], s[46:47]
	s_and_saveexec_b64 s[6:7], s[18:19]
	v_lshl_add_u32 v0, v0, 2, s95
	ds_write_b32 v0, v4
	s_or_b64 exec, exec, s[6:7]
	s_bcnt1_i32_b64 s6, s[44:45]
	v_cmp_eq_u32_e64 s[44:45], v3, v5
	s_add_i32 s8, s8, s6
	s_bcnt1_i32_b64 s6, vcc
	v_mbcnt_lo_u32_b32 v0, s44, 0
	s_add_i32 s9, s9, s6
	v_mbcnt_hi_u32_b32 v0, s45, v0
	v_add_u32_e32 v0, s9, v0
	v_cmp_gt_u32_e64 s[46:47], s4, v0
	v_cmp_gt_u32_e32 vcc, v3, v5
	s_and_b64 s[6:7], s[44:45], s[46:47]
	s_or_b64 s[6:7], vcc, s[6:7]
	s_mov_b64 vcc, s[6:7]
	s_nop 1
	v_mbcnt_lo_u32_b32 v0, vcc_lo, 0
	v_mbcnt_hi_u32_b32 v0, vcc_hi, v0
	v_add_u32_e32 v0, s8, v0
	v_cmp_gt_u32_e32 vcc, s75, v0
	s_and_b64 s[8:9], s[6:7], vcc
	s_and_saveexec_b64 s[6:7], s[8:9]
	v_lshl_add_u32 v0, v0, 2, s95
	ds_write_b32 v0, v2
	s_or_b64 exec, exec, s[6:7]
